# attention: both slots' DMA issue spread into QK segments (second slot's moved to next iteration's first QK, tail issues last V tile)
# speedup vs baseline: 1.0220x; 1.0032x over previous
; __device__ __forceinline__ unsigned cvtpk(float lo, float hi) { unsigned r; asm volatile("v_cvt_pk_bf16_f32 %0, %1, %2" : "=v"(r) : "v"(lo), "v"(hi)); return r; }
; __device__ __forceinline__ int v_st(int k, int c) { const int kk = (k & ~0xC) | ((k & 4) << 1) | ((k & 8) >> 1); return ((kk >> 3) * 4 + (c >> 5)) * 512 + ((kk & 7) * 32 + (c & 31)) * 2; }
; template <bool HALF> __device__ __forceinline__ void dense_body(const bf16_t* __restrict__ Qb, const bf16_t* __restrict__ Kh, const bf16_t* __restrict__ Vh, ...
;     ...
; #pragma unroll
;     for (int d0 = 0; d0 < NQ; ++d0) { u32x4 w;
; #pragma unroll
;       for (int j = 0; j < 4; ++j) w[j] = cvtpk(qf[d0][2 * j], qf[d0][2 * j + 1]);
;       qr[d0] = *reinterpret_cast<bf16x8*>(&w); } }
;   const int sr = tid >> 4, sc = (tid & 15) * 8, vst0 = v_st(sr, sc), vst1 = v_st(32 + sr, sc);
;   const int vb0 = (int)(uintptr_t)V_lds + v_rd_base(lane);
;   struct { bf16x8 vs0, vs1, ks0, ks1; } sr_[2];
;   const unsigned ko0 = (unsigned)(sr * LDKK + sc) * 2u, ko1 = ko0 + 32u * LDKK * 2u, vo0 = (unsigned)(sr * LDKV + sc) * 2u, vo1 = vo0 + 32u * LDKV * 2u;
;     ...
;   f32x16 pA0, pA1, pB0, pB1; float mnA, mnB, alA, alB; bf16x8 pa0, pa1, pa2, pa3; const int NT = seq / KVBLK;
;   const char* Kl0 = (const char*)K_lds; const char* Kl1 = (const char*)(K_lds + SHM_K);
;   constexpr int SE = 0, SO = 1;
;   SLOAD(SE, 0); asm volatile("s_waitcnt vmcnt(0)" ::: "memory"); SWRITE(0, SE); __syncthreads();
;   qkt<HALF>(pA0, pA1, Kl0, qr, r32, hi, koff); partialSM(pA0, pA1, m_reg, mnA, alA);
;   SLOAD(SO, KVBLK); if (2 < NT) SLOAD(SE, 2 * KVBLK);
; template <bool HALF> __device__ __forceinline__ void unit(const P& p, int l, int u, LAS char* lds, int tid) {
;     ...
;   if (u < 512) { hq = ((u >> 8) << 3) + (u & 7); qrow = CTXL + ((u >> 3) & 31) * 256; nk = NTOK; } else { hq = u - 512; qrow = 0; nk = CTXL; }
;   const int kvh = hq < 8 ? (hq >> 2) : 2 + ((hq - 8) >> 1);
;   const bf16_t* Qb = WSP(bf16_t, WS_PROJ) + (size_t)qrow * INW + (hq < 8 ? C_AQ + hq * 128 : C_DQ + (hq - 8) * 64);
;   const bf16_t* Kh = WSP(bf16_t, WS_KALL) + kvh * 128;
;   const bf16_t* Vh = WSP(bf16_t, WS_PROJ) + (kvh < 2 ? C_AV + kvh * 128 : C_DV + (kvh - 2) * 128);
;   bf16_t* Obf = !HALF ? WSP(bf16_t, WS_MIX) + (size_t)qrow * DM + 512 + hq * 128 : nullptr;
;   float* Of = !HALF ? nullptr : WSP(float, WS_DTMP) + (size_t)qrow * 1024 + (hq - 8) * 128;
.LBB0_424:
	s_ashr_i32 s6, s2, 2
	s_add_i32 s2, s2, -8
	s_lshr_b32 s2, s2, 1
	s_add_i32 s7, s2, 2
	s_and_b64 s[2:3], s[20:21], exec
	s_cselect_b32 s3, s6, s7
	s_lshl_b32 s2, s3, 7
	s_cmp_lt_i32 s3, 2
	s_movk_i32 s3, 0x1100
	s_cselect_b32 s3, s3, 0x1500
	s_add_i32 s6, s3, s2
	s_ashr_i32 s3, s2, 31
	s_lshl_b64 s[20:21], s[2:3], 1
	s_add_u32 s34, s44, s20
	v_cvt_pk_bf16_f32 v118, v122, v36
	v_cvt_pk_bf16_f32 v119, v123, v37
	v_cvt_pk_bf16_f32 v120, v120, v28
	v_cvt_pk_bf16_f32 v121, v121, v29
	v_cvt_pk_bf16_f32 v126, v114, v32
	v_cvt_pk_bf16_f32 v127, v115, v33
	v_cvt_pk_bf16_f32 v128, v112, v24
	v_cvt_pk_bf16_f32 v129, v113, v25
	v_cvt_pk_bf16_f32 v122, v108, v26
	v_cvt_pk_bf16_f32 v123, v109, v27
	v_cvt_pk_bf16_f32 v124, v106, v20
	v_cvt_pk_bf16_f32 v125, v107, v21
	v_cvt_pk_bf16_f32 v114, v104, v22
	v_cvt_pk_bf16_f32 v115, v105, v23
	v_cvt_pk_bf16_f32 v116, v74, v16
	v_cvt_pk_bf16_f32 v117, v75, v17
	v_ashrrev_i32_e32 v16, 4, v142
	v_lshlrev_b32_e32 v17, 3, v142
	s_movk_i32 s2, 0x300
	s_addc_u32 s35, s45, s21
	s_ashr_i32 s7, s6, 31
	v_cvt_pk_bf16_f32 v110, v72, v18
	v_and_b32_e32 v18, 0x78, v17
	v_mul_lo_u32 v0, v16, s2
	s_movk_i32 s2, 0x1800
	s_lshl_b64 s[22:23], s[6:7], 1
	v_cvt_pk_bf16_f32 v111, v73, v19
	v_cvt_pk_bf16_f32 v112, v70, v12
	v_cvt_pk_bf16_f32 v113, v71, v13
	v_cvt_pk_bf16_f32 v106, v68, v14
	v_cvt_pk_bf16_f32 v107, v69, v15
	v_cvt_pk_bf16_f32 v108, v6, v8
	v_or_b32_e32 v8, v0, v18
	v_mul_lo_u32 v0, v16, s2
	s_add_u32 s38, s30, s22
	v_or_b32_e32 v0, v0, v18
	s_addc_u32 s39, s31, s23
	v_lshlrev_b32_e32 v50, 1, v0
	v_cvt_pk_bf16_f32 v109, v7, v9
	v_cvt_pk_bf16_f32 v102, v4, v10
	v_cvt_pk_bf16_f32 v103, v5, v11
	v_cvt_pk_bf16_f32 v104, v2, v64
	v_cvt_pk_bf16_f32 v105, v1, v65
	v_cvt_pk_bf16_f32 v98, v40, v46
	v_cvt_pk_bf16_f32 v99, v39, v47
	v_cvt_pk_bf16_f32 v100, v34, v42
	v_cvt_pk_bf16_f32 v101, v31, v43
	v_add_u32_e32 v48, 0x60000, v50
	v_readlane_b32 s52, v252, 4
	s_nop 3
	v_and_b32_e32 v134, 63, v142
	v_lshrrev_b32_e32 v135, 4, v134
	v_and_b32_e32 v136, 15, v134
	s_lshl_b32 s53, s52, 3
	v_add_u32_e32 v137, s53, v135
	v_xor_b32_e32 v138, v136, v135
	v_mul_u32_u24_e32 v130, 0x600, v137
	v_lshl_add_u32 v130, v138, 4, v130
	v_add_u32_e32 v139, 4, v135
	v_xor_b32_e32 v138, v136, v139
	v_add_u32_e32 v137, 4, v137
	v_mul_u32_u24_e32 v131, 0x600, v137
	v_lshl_add_u32 v131, v138, 4, v131
	v_bfe_u32 v135, v134, 2, 3
	v_add_u32_e32 v135, s53, v135
	v_and_b32_e32 v136, 4, v135
	v_and_b32_e32 v137, 8, v135
	v_and_b32_e32 v135, 0xfffffff3, v135
	v_lshl_or_b32 v135, v136, 1, v135
	v_lshrrev_b32_e32 v137, 1, v137
	v_or_b32_e32 v135, v135, v137
	v_mul_u32_u24_e32 v132, 0x3000, v135
	v_lshrrev_b32_e32 v136, 5, v134
	v_lshl_add_u32 v132, v136, 6, v132
	v_and_b32_e32 v136, 3, v134
	v_lshl_add_u32 v132, v136, 4, v132
	v_add_u32_e32 v133, 0x80, v132
	v_mov_b32_e32 v140, v132
	v_mov_b32_e32 v141, v133
	s_lshl_b32 s53, s52, 11
	s_add_i32 s52, s53, 0x8000
	s_add_i32 m0, s52, 0x0
	s_nop 0
	global_load_lds_dwordx4 v130, s[34:35]
	s_add_i32 m0, s52, 0x400
	s_nop 0
	global_load_lds_dwordx4 v131, s[34:35]
	s_add_i32 m0, s53, 0x0
	s_nop 0
	global_load_lds_dwordx4 v132, s[38:39]
	s_add_i32 m0, s53, 0x400
	s_nop 0
	global_load_lds_dwordx4 v133, s[38:39]
	s_add_u32 s48, s34, 0x18000
	s_addc_u32 s49, s35, 0
	s_add_u32 s50, s38, 0xc0000
	s_addc_u32 s51, s39, 0
	s_add_i32 m0, s52, 0x4000
	s_nop 0
	global_load_lds_dwordx4 v130, s[48:49]
	s_add_i32 m0, s52, 0x4400
	s_nop 0
	global_load_lds_dwordx4 v131, s[48:49]
	s_add_i32 m0, s53, 0x4000
	s_nop 0
	global_load_lds_dwordx4 v132, s[50:51]
	s_add_i32 m0, s53, 0x4400
	s_nop 0
	global_load_lds_dwordx4 v133, s[50:51]
	s_add_u32 s48, s48, 0x18000
	s_addc_u32 s49, s49, 0
	s_add_u32 s50, s50, 0xc0000
	s_addc_u32 s51, s51, 0
	v_lshlrev_b32_e32 v52, 1, v8
	v_add_u32_e32 v54, 0xc000, v52
	v_and_b32_e32 v20, 0xfffff0, v16
	v_lshlrev_b32_e32 v21, 1, v16
	v_lshrrev_b32_e32 v22, 1, v16
	v_and_b32_e32 v23, 3, v16
	v_add_u32_e32 v24, 32, v16
	v_and_or_b32 v20, v21, 8, v20
	v_and_or_b32 v21, v22, 4, v23
	v_and_b32_e32 v22, 0xfffff0, v24
	v_lshlrev_b32_e32 v23, 1, v24
	v_bfe_u32 v17, v17, 5, 2
	v_lshrrev_b32_e32 v20, 1, v20
	v_and_or_b32 v22, v23, 8, v22
	v_lshlrev_b32_e32 v18, 1, v18
	v_or_b32_e32 v20, v20, v17
	v_lshrrev_b32_e32 v22, 1, v22
	v_lshlrev_b32_e32 v21, 6, v21
	v_and_b32_e32 v25, 48, v18
	v_lshlrev_b32_e32 v20, 9, v20
	v_or_b32_e32 v17, v22, v17
	v_or3_b32 v20, v20, v21, v25
	v_lshlrev_b32_e32 v17, 9, v17
	v_or3_b32 v17, v17, v21, v25
	v_add_u32_e32 v205, 0, v20
	v_and_b32_e32 v19, 0x70, v142
	v_lshlrev_b32_e32 v16, 8, v16
	v_add_u32_e32 v206, 0, v17
	s_waitcnt vmcnt(0)
	v_bitop3_b32 v16, v18, v16, v19 bitop3:0xde
	v_lshlrev_b32_e32 v0, 8, v24
	v_bitop3_b32 v0, v18, v0, v19 bitop3:0xde
	v_add_u32_e32 v207, 0, v16
	v_add_u32_e32 v208, 0, v0
	v_lshlrev_b32_e32 v0, 4, v197
	v_lshlrev_b32_e32 v8, 8, v197
	v_and_b32_e32 v9, 0x70, v0
	v_bitop3_b32 v0, v96, v8, v9 bitop3:0xde
	v_add_u32_e32 v209, 0, v0
	s_waitcnt lgkmcnt(0)
	s_barrier
; __device__ __forceinline__ void partialSM(f32x16& p0, f32x16& p1, float& m_reg, float& mn, float& alpha) {
;   constexpr float C = SCALE * 1.4426950408889634f;
;   float pmax = p0[0]; for (int r = 1; r < 16; ++r) pmax = fmaxf(pmax, p0[r]); for (int r = 0; r < 16; ++r) pmax = fmaxf(pmax, p1[r]);
;   { auto rr = __builtin_amdgcn_permlane32_swap(__float_as_uint(pmax), __float_as_uint(pmax), false, false);
;     pmax = fmaxf(__uint_as_float(rr[0]), __uint_as_float(rr[1])); }
;   if (__builtin_expect(__all(pmax - m_reg <= THR / SCALE), 1)) { mn = m_reg; alpha = 1.f; }
;   else { mn = fmaxf(m_reg, pmax); alpha = __builtin_amdgcn_exp2f((m_reg - mn) * C); m_reg = mn; }
;   float mnC = -mn * C;
;   for (int r = 0; r < 16; ++r) p0[r] = fmaf(p0[r], C, mnC); for (int r = 0; r < 16; ++r) p1[r] = fmaf(p1[r], C, mnC);
;   for (int r = 0; r < 16; ++r) p0[r] = __builtin_amdgcn_exp2f(p0[r]);
; }
; template <bool HALF> __device__ __forceinline__ void qkt(f32x16& p0, f32x16& p1, const char* Ks, const bf16x8* qr, int r32, int hi, int koff) {
;   p0 = f32x16{}; p1 = f32x16{};
;   for (int d0 = 0; d0 < (HALF ? 4 : 8); ++d0) { int cb = (d0 * 16 + hi * 8) * 2 + koff;
;     bf16x8 b0 = *reinterpret_cast<const bf16x8*>(Ks + KSWZ(r32, cb));
;     bf16x8 b1 = *reinterpret_cast<const bf16x8*>(Ks + KSWZ(32 + r32, cb));
;     p0 = __builtin_amdgcn_mfma_f32_32x32x16_bf16(b0, qr[d0], p0, 0, 0, 0);
;     p1 = __builtin_amdgcn_mfma_f32_32x32x16_bf16(b1, qr[d0], p1, 0, 0, 0); }
	ds_read_b128 v[0:3], v209 offset:32768
	ds_read_b128 v[4:7], v209 offset:40960
	s_waitcnt lgkmcnt(1)
	v_mfma_f32_32x32x16_bf16 v[16:31], v[0:3], v[118:121], 0
	v_or_b32_e32 v0, 32, v96
	v_bitop3_b32 v0, v0, v8, v9 bitop3:0xde
	v_add_u32_e32 v221, 0, v0
	v_and_b32_e32 v76, 63, v142
	v_and_b32_e32 v10, 0x3fffffc0, v142
	s_add_i32 s46, 0, 0x10000
	v_lshl_add_u32 v200, v10, 2, s46
	s_waitcnt lgkmcnt(0)
	v_mfma_f32_32x32x16_bf16 v[32:47], v[4:7], v[118:121], 0
	ds_read_b128 v[0:3], v221 offset:32768
	ds_read_b128 v[4:7], v221 offset:40960
	v_lshlrev_b32_e32 v10, 3, v76
	s_add_u32 s6, s34, 0x18000
	s_addc_u32 s7, s35, 0
	s_add_u32 s16, s38, 0xc0000
	s_addc_u32 s17, s39, 0
	s_mov_b32 s64, s65
	s_waitcnt lgkmcnt(1)
	v_mfma_f32_32x32x16_bf16 v[16:31], v[0:3], v[126:129], v[16:31]
	v_or_b32_e32 v0, 64, v96
	v_bitop3_b32 v0, v0, v8, v9 bitop3:0xde
	v_add_u32_e32 v222, 0, v0
	s_mov_b32 s66, s65
	s_mov_b32 s67, s65
	s_mov_b32 s68, s65
	s_mov_b32 s69, s65
	s_waitcnt lgkmcnt(0)
	v_mfma_f32_32x32x16_bf16 v[32:47], v[4:7], v[126:129], v[32:47]
	ds_read_b128 v[0:3], v222 offset:32768
	ds_read_b128 v[4:7], v222 offset:40960
	s_mov_b32 s70, s65
	s_mov_b32 s71, s65
	s_mov_b32 s72, s65
	s_mov_b32 s73, s65
	s_mov_b32 s74, s65
	s_mov_b32 s75, s65
	s_waitcnt lgkmcnt(1)
	v_mfma_f32_32x32x16_bf16 v[16:31], v[0:3], v[122:125], v[16:31]
	v_or_b32_e32 v0, 0x60, v96
	v_bitop3_b32 v0, v0, v8, v9 bitop3:0xde
	v_add_u32_e32 v210, 0, v0
	s_mov_b32 s76, s65
	s_mov_b32 s77, s65
	s_mov_b32 s78, s65
	s_mov_b32 s79, s65
	s_waitcnt lgkmcnt(0)
	v_mfma_f32_32x32x16_bf16 v[32:47], v[4:7], v[122:125], v[32:47]
	ds_read_b128 v[0:3], v210 offset:32768
	ds_read_b128 v[4:7], v210 offset:40960
	v_mov_b32_e32 v51, v97
	v_mov_b32_e32 v49, v97
	v_mov_b32_e32 v53, v97
	v_mov_b32_e32 v55, v97
	v_lshl_add_u64 v[180:181], s[22:23], 0, v[50:51]
	v_lshl_add_u64 v[182:183], s[22:23], 0, v[48:49]
	s_waitcnt lgkmcnt(1)
	v_mfma_f32_32x32x16_bf16 v[16:31], v[0:3], v[114:117], v[16:31]
	v_or_b32_e32 v0, 0x80, v96
	v_bitop3_b32 v0, v0, v8, v9 bitop3:0xde
	v_add_u32_e32 v211, 0, v0
	ds_read_b128 v[0:3], v211 offset:32768
	v_lshl_add_u64 v[184:185], s[20:21], 0, v[52:53]
	v_lshl_add_u64 v[186:187], s[20:21], 0, v[54:55]
	s_mov_b32 s2, 4
	s_waitcnt lgkmcnt(1)
	v_mfma_f32_32x32x16_bf16 v[32:47], v[4:7], v[114:117], v[32:47]
	ds_read_b128 v[4:7], v211 offset:40960
	v_cmp_gt_u32_e64 s[40:41], 32, v76
	v_lshl_add_u32 v201, v197, 2, v200
	v_mov_b32_e32 v202, 0
	s_waitcnt lgkmcnt(1)
	v_mfma_f32_32x32x16_bf16 v[16:31], v[0:3], v[110:113], v[16:31]
	v_lshlrev_b32_e32 v0, 4, v76
	v_and_b32_e32 v0, 0xc0, v0
	v_and_or_b32 v11, v10, 24, v0
	v_or_b32_e32 v0, 0xa0, v96
	v_bitop3_b32 v0, v0, v8, v9 bitop3:0xde
	v_add_u32_e32 v223, 0, v0
	v_and_b32_e32 v10, 0x100, v10
	s_waitcnt lgkmcnt(0)
	v_mfma_f32_32x32x16_bf16 v[32:47], v[4:7], v[110:113], v[32:47]
	ds_read_b128 v[0:3], v223 offset:32768
	ds_read_b128 v[4:7], v223 offset:40960
	s_add_u32 s6, s34, 0x30000
	s_addc_u32 s7, s35, 0
	s_waitcnt lgkmcnt(1)
	v_mfma_f32_32x32x16_bf16 v[16:31], v[0:3], v[106:109], v[16:31]
	v_lshlrev_b32_e32 v0, 1, v76
	v_and_b32_e32 v12, 32, v0
	v_or_b32_e32 v0, 0xc0, v96
	v_bitop3_b32 v0, v0, v8, v9 bitop3:0xde
	v_add_u32_e32 v225, 0, v0
	ds_read_b128 v[0:3], v225 offset:32768
	v_or3_b32 v77, v11, v12, v10
	s_waitcnt lgkmcnt(1)
	v_mfma_f32_32x32x16_bf16 v[32:47], v[4:7], v[106:109], v[32:47]
	ds_read_b128 v[4:7], v225 offset:40960
	v_add_u32_e32 v204, 0, v77
	s_waitcnt lgkmcnt(1)
	v_mfma_f32_32x32x16_bf16 v[16:31], v[0:3], v[102:105], v[16:31]
	v_or_b32_e32 v0, 0xe0, v96
	v_bitop3_b32 v0, v0, v8, v9 bitop3:0xde
	v_add_u32_e32 v224, 0, v0
	ds_read_b128 v[0:3], v224 offset:32768
	ds_read_b128 v[72:75], v224 offset:40960
	s_add_u32 s6, s38, 0x180000
	s_addc_u32 s7, s39, 0
	s_waitcnt lgkmcnt(2)
	v_mfma_f32_32x32x16_bf16 v[32:47], v[4:7], v[102:105], v[32:47]
	s_waitcnt lgkmcnt(1)
	v_mfma_f32_32x32x16_bf16 v[16:31], v[0:3], v[98:101], v[16:31]
	v_mov_b64_e32 v[0:1], s[64:65]
	v_mov_b64_e32 v[14:15], s[78:79]
	v_mov_b64_e32 v[2:3], s[66:67]
	v_mov_b64_e32 v[4:5], s[68:69]
	v_mov_b64_e32 v[6:7], s[70:71]
	v_mov_b64_e32 v[8:9], s[72:73]
	v_mov_b64_e32 v[10:11], s[74:75]
	s_waitcnt lgkmcnt(0)
	v_mfma_f32_32x32x16_bf16 v[32:47], v[72:75], v[98:101], v[32:47]
	s_nop 2
	v_max_f32_e32 v72, v17, v17
	v_max_f32_e32 v73, v16, v16
	v_max_f32_e32 v72, v73, v72
	v_max3_f32 v72, v72, v18, v19
	v_max3_f32 v72, v72, v20, v21
	v_max3_f32 v72, v72, v22, v23
	v_max3_f32 v72, v72, v24, v25
	v_max3_f32 v72, v72, v26, v27
	v_max3_f32 v72, v72, v28, v29
	v_max3_f32 v72, v72, v30, v31
	v_max3_f32 v72, v72, v32, v33
	v_max3_f32 v72, v72, v34, v35
	v_max3_f32 v72, v72, v36, v37
	v_max3_f32 v72, v72, v38, v39
	v_max3_f32 v72, v72, v40, v41
	v_max3_f32 v72, v72, v42, v43
	v_max3_f32 v72, v72, v44, v45
	v_max3_f32 v72, v72, v46, v47
	v_mov_b32_e32 v73, v72
	s_nop 1
	v_permlane32_swap_b32_e32 v72, v73
	v_max_f32_e32 v73, v73, v73
	v_max_f32_e32 v72, v72, v72
	v_max_f32_e32 v72, v72, v73
	v_add_f32_e32 v73, 0x7149f2ca, v72
	v_cmp_ge_f32_e32 vcc, s87, v73
	s_cmp_eq_u64 vcc, exec
	v_max_f32_e32 v56, 0xf149f2ca, v72
	s_cselect_b64 vcc, -1, 0
	v_cndmask_b32_e32 v170, v56, v217, vcc
	v_sub_f32_e32 v57, 0xf149f2ca, v56
	v_mul_f32_e32 v56, 0xbe0293ee, v170
	v_fmamk_f32 v16, v16, 0x3e0293ee, v56
	v_exp_f32_e32 v163, v16
	v_fmamk_f32 v16, v17, 0x3e0293ee, v56
	v_exp_f32_e32 v177, v16
	v_fmamk_f32 v16, v18, 0x3e0293ee, v56
	v_exp_f32_e32 v164, v16
	v_fmamk_f32 v16, v19, 0x3e0293ee, v56
	v_exp_f32_e32 v188, v16
	v_fmamk_f32 v16, v20, 0x3e0293ee, v56
	v_exp_f32_e32 v176, v16
	v_fmamk_f32 v16, v21, 0x3e0293ee, v56
	v_exp_f32_e32 v189, v16
	v_fmamk_f32 v16, v22, 0x3e0293ee, v56
; __device__ __forceinline__ void partialSM(f32x16& p0, f32x16& p1, float& m_reg, float& mn, float& alpha) {
;     ...
;   float mnC = -mn * C;
;   for (int r = 0; r < 16; ++r) p0[r] = fmaf(p0[r], C, mnC); for (int r = 0; r < 16; ++r) p1[r] = fmaf(p1[r], C, mnC);
;   for (int r = 0; r < 16; ++r) p0[r] = __builtin_amdgcn_exp2f(p0[r]);
; }
; __device__ __forceinline__ void finishSM(f32x16& p0, f32x16& p1, float alpha, float& l_reg, bf16x8& pa0, bf16x8& pa1, bf16x8& pa2, bf16x8& pa3) {
;   for (int r = 0; r < 16; ++r) p1[r] = __builtin_amdgcn_exp2f(p1[r]);
;   float ps = 0; for (int r = 0; r < 16; ++r) ps += p0[r]; for (int r = 0; r < 16; ++r) ps += p1[r];
;   { auto rr = __builtin_amdgcn_permlane32_swap(__float_as_uint(ps), __float_as_uint(ps), false, false);
;     ps = __uint_as_float(rr[0]) + __uint_as_float(rr[1]); }
;   l_reg = l_reg * alpha + ps;
;     ...
;   PK4(p0, 0, pa0); PK4(p0, 8, pa1); PK4(p1, 0, pa2); PK4(p1, 8, pa3);
;     ...
; }
; template <bool HALF> __device__ __forceinline__ void qkt(f32x16& p0, f32x16& p1, const char* Ks, const bf16x8* qr, int r32, int hi, int koff) {
;   p0 = f32x16{}; p1 = f32x16{};
;   for (int d0 = 0; d0 < (HALF ? 4 : 8); ++d0) { int cb = (d0 * 16 + hi * 8) * 2 + koff;
;     bf16x8 b0 = *reinterpret_cast<const bf16x8*>(Ks + KSWZ(r32, cb));
;     bf16x8 b1 = *reinterpret_cast<const bf16x8*>(Ks + KSWZ(32 + r32, cb));
;     p0 = __builtin_amdgcn_mfma_f32_32x32x16_bf16(b0, qr[d0], p0, 0, 0, 0);
;     p1 = __builtin_amdgcn_mfma_f32_32x32x16_bf16(b1, qr[d0], p1, 0, 0, 0); }
	v_exp_f32_e32 v165, v16
	v_fmamk_f32 v16, v23, 0x3e0293ee, v56
	v_exp_f32_e32 v175, v16
	v_fmamk_f32 v16, v24, 0x3e0293ee, v56
	v_mul_f32_e32 v57, 0x3e0293ee, v57
	v_exp_f32_e32 v166, v16
	v_fmamk_f32 v16, v25, 0x3e0293ee, v56
	v_exp_f32_e32 v57, v57
	v_exp_f32_e32 v173, v16
	v_fmamk_f32 v16, v26, 0x3e0293ee, v56
	v_exp_f32_e32 v167, v16
	v_fmamk_f32 v16, v27, 0x3e0293ee, v56
	v_exp_f32_e32 v174, v16
	v_fmamk_f32 v16, v28, 0x3e0293ee, v56
	v_exp_f32_e32 v168, v16
	v_fmamk_f32 v16, v29, 0x3e0293ee, v56
	v_pk_fma_f32 v[146:147], v[46:47], s[10:11], v[56:57] op_sel_hi:[1,0,0]
	v_pk_fma_f32 v[152:153], v[44:45], s[10:11], v[56:57] op_sel_hi:[1,0,0]
	v_pk_fma_f32 v[156:157], v[42:43], s[10:11], v[56:57] op_sel_hi:[1,0,0]
	v_pk_fma_f32 v[148:149], v[40:41], s[10:11], v[56:57] op_sel_hi:[1,0,0]
	v_pk_fma_f32 v[150:151], v[38:39], s[10:11], v[56:57] op_sel_hi:[1,0,0]
	v_pk_fma_f32 v[154:155], v[36:37], s[10:11], v[56:57] op_sel_hi:[1,0,0]
	v_pk_fma_f32 v[158:159], v[34:35], s[10:11], v[56:57] op_sel_hi:[1,0,0]
	v_pk_fma_f32 v[160:161], v[32:33], s[10:11], v[56:57] op_sel_hi:[1,0,0]
	v_exp_f32_e32 v171, v16
	v_fmamk_f32 v16, v30, 0x3e0293ee, v56
	v_fmac_f32_e32 v56, 0x3e0293ee, v31
	v_exp_f32_e32 v169, v16
	v_exp_f32_e32 v172, v56
	v_mov_b64_e32 v[12:13], s[76:77]
	v_cndmask_b32_e64 v226, v57, 1.0, vcc
	s_add_i32 s34, 0, 0x4000
	v_mov_b64_e32 v[62:63], v[14:15]
	v_mov_b64_e32 v[46:47], v[14:15]
	v_mov_b64_e32 v[30:31], v[14:15]
	v_add_u32_e32 v203, s34, v77
	v_mov_b64_e32 v[60:61], v[12:13]
	v_mov_b64_e32 v[58:59], v[10:11]
	v_mov_b64_e32 v[56:57], v[8:9]
	v_mov_b64_e32 v[54:55], v[6:7]
	v_mov_b64_e32 v[52:53], v[4:5]
	v_mov_b64_e32 v[50:51], v[2:3]
	v_mov_b64_e32 v[48:49], v[0:1]
	v_mov_b64_e32 v[44:45], v[12:13]
	v_mov_b64_e32 v[42:43], v[10:11]
	v_mov_b64_e32 v[40:41], v[8:9]
	v_mov_b64_e32 v[38:39], v[6:7]
	v_mov_b64_e32 v[36:37], v[4:5]
	v_mov_b64_e32 v[34:35], v[2:3]
	v_mov_b64_e32 v[32:33], v[0:1]
	v_mov_b64_e32 v[28:29], v[12:13]
	v_mov_b64_e32 v[26:27], v[10:11]
	v_mov_b64_e32 v[24:25], v[8:9]
	v_mov_b64_e32 v[22:23], v[6:7]
	v_mov_b64_e32 v[20:21], v[4:5]
	v_mov_b64_e32 v[18:19], v[2:3]
	v_mov_b64_e32 v[16:17], v[0:1]
	s_waitcnt lgkmcnt(0)
	s_barrier
	s_add_i32 m0, s52, 0x0
	s_nop 0
	global_load_lds_dwordx4 v130, s[48:49]
	s_add_i32 m0, s52, 0x400
	s_nop 0
	global_load_lds_dwordx4 v131, s[48:49]
	s_add_u32 s48, s48, 0x18000
	s_addc_u32 s49, s49, 0
	s_mov_b32 s54, 0
.LBB0_425:
	ds_read_b128 v[64:67], v209 offset:49152
	ds_read_b128 v[68:71], v209 offset:57344
	ds_read_b128 v[190:193], v221 offset:49152
	ds_read_b128 v[228:231], v221 offset:57344
	v_add_f32_e32 v162, 0, v163
	v_add_f32_e32 v162, v177, v162
	s_waitcnt lgkmcnt(3)
	v_mfma_f32_32x32x16_bf16 v[80:95], v[64:67], v[118:121], 0
	v_add_f32_e32 v162, v164, v162
	v_add_f32_e32 v162, v188, v162
	v_add_f32_e32 v162, v176, v162
	v_add_f32_e32 v162, v189, v162
	v_add_f32_e32 v162, v165, v162
	v_add_f32_e32 v162, v175, v162
	v_add_f32_e32 v162, v166, v162
	s_waitcnt lgkmcnt(2)
	v_mfma_f32_32x32x16_bf16 v[64:79], v[68:71], v[118:121], 0
	v_add_f32_e32 v162, v173, v162
	v_add_f32_e32 v162, v167, v162
	v_add_f32_e32 v162, v174, v162
	v_exp_f32_e32 v160, v160
	v_add_f32_e32 v162, v168, v162
	v_exp_f32_e32 v161, v161
	v_add_f32_e32 v162, v171, v162
	s_waitcnt lgkmcnt(1)
	v_mfma_f32_32x32x16_bf16 v[80:95], v[190:193], v[126:129], v[80:95]
	s_cmp_eq_u32 s54, 0
	s_cbranch_scc1 .Lmv_f
	s_add_i32 m0, s52, 0x0
	s_nop 0
	global_load_lds_dwordx4 v130, s[48:49]
	s_add_i32 m0, s52, 0x400
	s_nop 0
	global_load_lds_dwordx4 v131, s[48:49]
	s_add_u32 s48, s48, 0x18000
	s_addc_u32 s49, s49, 0
	s_add_i32 m0, s53, 0x4000
	s_nop 0
	global_load_lds_dwordx4 v132, s[50:51]
	s_add_i32 m0, s53, 0x4400
	s_nop 0
	global_load_lds_dwordx4 v133, s[50:51]
	s_add_u32 s50, s50, 0xc0000
	s_addc_u32 s51, s51, 0
.Lmv_f:
	v_exp_f32_e32 v158, v158
	v_add_f32_e32 v162, v169, v162
	v_exp_f32_e32 v159, v159
	v_add_f32_e32 v162, v172, v162
	v_exp_f32_e32 v154, v154
	v_add_f32_e32 v162, v160, v162
	v_exp_f32_e32 v155, v155
	s_waitcnt lgkmcnt(0)
	v_mfma_f32_32x32x16_bf16 v[64:79], v[228:231], v[126:129], v[64:79]
	ds_read_b128 v[190:193], v222 offset:49152
	ds_read_b128 v[228:231], v222 offset:57344
	v_add_f32_e32 v162, v161, v162
	v_exp_f32_e32 v150, v150
	v_add_f32_e32 v162, v158, v162
	v_exp_f32_e32 v151, v151
	v_add_f32_e32 v162, v159, v162
	v_exp_f32_e32 v148, v148
	s_waitcnt lgkmcnt(1)
	v_mfma_f32_32x32x16_bf16 v[80:95], v[190:193], v[122:125], v[80:95]
	v_add_f32_e32 v162, v154, v162
	v_exp_f32_e32 v149, v149
	v_add_f32_e32 v162, v155, v162
	v_exp_f32_e32 v156, v156
	v_add_f32_e32 v162, v150, v162
	v_exp_f32_e32 v157, v157
	v_add_f32_e32 v162, v151, v162
	s_waitcnt lgkmcnt(0)
	v_mfma_f32_32x32x16_bf16 v[64:79], v[228:231], v[122:125], v[64:79]
	ds_read_b128 v[190:193], v210 offset:49152
	ds_read_b128 v[228:231], v210 offset:57344
	v_exp_f32_e32 v152, v152
	v_add_f32_e32 v162, v148, v162
	v_exp_f32_e32 v153, v153
	v_add_f32_e32 v162, v149, v162
	v_exp_f32_e32 v146, v146
	v_add_f32_e32 v162, v156, v162
	s_waitcnt lgkmcnt(1)
	v_mfma_f32_32x32x16_bf16 v[80:95], v[190:193], v[114:117], v[80:95]
	v_exp_f32_e32 v147, v147
	v_add_f32_e32 v162, v157, v162
	v_add_f32_e32 v162, v152, v162
	v_add_f32_e32 v162, v153, v162
	v_add_f32_e32 v162, v146, v162
	v_add_f32_e32 v227, v147, v162
	s_waitcnt lgkmcnt(0)
	v_mfma_f32_32x32x16_bf16 v[64:79], v[228:231], v[114:117], v[64:79]
	ds_read_b128 v[190:193], v211 offset:49152
	ds_read_b128 v[228:231], v211 offset:57344
	s_waitcnt lgkmcnt(1)
	v_mfma_f32_32x32x16_bf16 v[80:95], v[190:193], v[110:113], v[80:95]
	s_waitcnt lgkmcnt(0)
; #define SBAR() __builtin_amdgcn_sched_barrier(0)
; __device__ __forceinline__ void partialSM(f32x16& p0, f32x16& p1, float& m_reg, float& mn, float& alpha) {
;     ...
;   float pmax = p0[0]; for (int r = 1; r < 16; ++r) pmax = fmaxf(pmax, p0[r]); for (int r = 0; r < 16; ++r) pmax = fmaxf(pmax, p1[r]);
;   { auto rr = __builtin_amdgcn_permlane32_swap(__float_as_uint(pmax), __float_as_uint(pmax), false, false);
;     pmax = fmaxf(__uint_as_float(rr[0]), __uint_as_float(rr[1])); }
;   if (__builtin_expect(__all(pmax - m_reg <= THR / SCALE), 1)) { mn = m_reg; alpha = 1.f; }
;   else { mn = fmaxf(m_reg, pmax); alpha = __builtin_amdgcn_exp2f((m_reg - mn) * C); m_reg = mn; }
; template <int D0> __device__ __forceinline__ void pv_one(f32x16& od, int vb, bf16x8 pa0, bf16x8 pa1, bf16x8 pa2, bf16x8 pa3) {
;   const s16x4 l0 = tr_read<v_rd_off(D0, 0, 0)>(vb), h0 = tr_read<v_rd_off(D0, 0, 1)>(vb), l1 = tr_read<v_rd_off(D0, 1, 0)>(vb), h1 = tr_read<v_rd_off(D0, 1, 1)>(vb);
;   const s16x4 l2 = tr_read<v_rd_off(D0, 2, 0)>(vb), h2 = tr_read<v_rd_off(D0, 2, 1)>(vb), l3 = tr_read<v_rd_off(D0, 3, 0)>(vb), h3 = tr_read<v_rd_off(D0, 3, 1)>(vb);
;   asm volatile("s_waitcnt lgkmcnt(0)" ::: "memory"); SBAR();
;     ...
;   od = __builtin_amdgcn_mfma_f32_32x32x16_bf16(pa0, PK(l0, h0), od, 0, 0, 0);
;   od = __builtin_amdgcn_mfma_f32_32x32x16_bf16(pa1, PK(l1, h1), od, 0, 0, 0);
;   od = __builtin_amdgcn_mfma_f32_32x32x16_bf16(pa2, PK(l2, h2), od, 0, 0, 0);
;   od = __builtin_amdgcn_mfma_f32_32x32x16_bf16(pa3, PK(l3, h3), od, 0, 0, 0);
;     ...
; }
; __device__ __forceinline__ void pv_d0(f32x16* o, int vb, bf16x8 pa0, bf16x8 pa1, bf16x8 pa2, bf16x8 pa3) {
;   pv_one<0>(o[0], vb, pa0, pa1, pa2, pa3); pv_one<1>(o[1], vb, pa0, pa1, pa2, pa3); pv_one<2>(o[2], vb, pa0, pa1, pa2, pa3); pv_one<3>(o[3], vb, pa0, pa1, pa2, pa3);
	v_mfma_f32_32x32x16_bf16 v[64:79], v[228:231], v[110:113], v[64:79]
	ds_read_b128 v[190:193], v223 offset:49152
	ds_read_b128 v[228:231], v223 offset:57344
	s_waitcnt lgkmcnt(1)
	v_mfma_f32_32x32x16_bf16 v[80:95], v[190:193], v[106:109], v[80:95]
	s_waitcnt lgkmcnt(0)
	v_mfma_f32_32x32x16_bf16 v[64:79], v[228:231], v[106:109], v[64:79]
	ds_read_b128 v[190:193], v225 offset:49152
	ds_read_b128 v[228:231], v225 offset:57344
	s_waitcnt lgkmcnt(1)
	v_mfma_f32_32x32x16_bf16 v[80:95], v[190:193], v[102:105], v[80:95]
	s_waitcnt lgkmcnt(0)
	v_mfma_f32_32x32x16_bf16 v[64:79], v[228:231], v[102:105], v[64:79]
	ds_read_b128 v[190:193], v224 offset:49152
	ds_read_b128 v[228:231], v224 offset:57344
	v_cvt_pk_bf16_f32 v162, v163, v177
	v_cvt_pk_bf16_f32 v163, v164, v188
	v_cvt_pk_bf16_f32 v164, v176, v189
	v_cvt_pk_bf16_f32 v165, v165, v175
	v_cvt_pk_bf16_f32 v166, v166, v173
	v_cvt_pk_bf16_f32 v167, v167, v174
	s_waitcnt lgkmcnt(1)
	v_mfma_f32_32x32x16_bf16 v[80:95], v[190:193], v[98:101], v[80:95]
	v_permlane32_swap_b32_e32 v162, v164
	v_cvt_pk_bf16_f32 v168, v168, v171
	v_cvt_pk_bf16_f32 v169, v169, v172
	v_cvt_pk_bf16_f32 v172, v160, v161
	v_cvt_pk_bf16_f32 v173, v158, v159
	v_cvt_pk_bf16_f32 v174, v154, v155
	s_waitcnt lgkmcnt(0)
	v_mfma_f32_32x32x16_bf16 v[64:79], v[228:231], v[98:101], v[64:79]
	v_mov_b32_e32 v228, v227
	s_nop 1
	v_permlane32_swap_b32_e32 v227, v228
	v_cvt_pk_bf16_f32 v175, v150, v151
	v_cvt_pk_bf16_f32 v230, v148, v149
	v_cvt_pk_bf16_f32 v231, v156, v157
	v_cvt_pk_bf16_f32 v232, v152, v153
	v_cvt_pk_bf16_f32 v233, v146, v147
	v_permlane32_swap_b32_e32 v163, v165
	v_permlane32_swap_b32_e32 v166, v168
	v_permlane32_swap_b32_e32 v167, v169
	v_permlane32_swap_b32_e32 v172, v174
	v_permlane32_swap_b32_e32 v173, v175
	v_permlane32_swap_b32_e32 v230, v232
	v_permlane32_swap_b32_e32 v231, v233
	ds_read_b64_tr_b16 v[234:235], v204 offset:0
	ds_read_b64_tr_b16 v[236:237], v204 offset:0x800
	ds_read_b64_tr_b16 v[238:239], v204 offset:0x1000
	ds_read_b64_tr_b16 v[240:241], v204 offset:0x1800
	ds_read_b64_tr_b16 v[242:243], v204 offset:0x2000
	ds_read_b64_tr_b16 v[244:245], v204 offset:0x2800
	ds_read_b64_tr_b16 v[246:247], v204 offset:0x3000
	ds_read_b64_tr_b16 v[248:249], v204 offset:0x3800
	s_waitcnt lgkmcnt(0)
	s_nop 0
	v_mfma_f32_32x32x16_bf16 v[0:15], v[162:165], v[234:237], v[0:15]
	ds_read_b64_tr_b16 v[234:235], v204 offset:0x200
	ds_read_b64_tr_b16 v[236:237], v204 offset:0xa00
	v_mfma_f32_32x32x16_bf16 v[0:15], v[166:169], v[238:241], v[0:15]
	ds_read_b64_tr_b16 v[238:239], v204 offset:0x1200
	ds_read_b64_tr_b16 v[240:241], v204 offset:0x1a00
	v_mfma_f32_32x32x16_bf16 v[0:15], v[172:175], v[242:245], v[0:15]
	ds_read_b64_tr_b16 v[242:243], v204 offset:0x2200
	ds_read_b64_tr_b16 v[244:245], v204 offset:0x2a00
	v_mfma_f32_32x32x16_bf16 v[0:15], v[230:233], v[246:249], v[0:15]
	ds_read_b64_tr_b16 v[246:247], v204 offset:0x3200
	ds_read_b64_tr_b16 v[248:249], v204 offset:0x3a00
	s_waitcnt lgkmcnt(0)
	v_mfma_f32_32x32x16_bf16 v[48:63], v[162:165], v[234:237], v[48:63]
	ds_read_b64_tr_b16 v[234:235], v204 offset:0x400
	ds_read_b64_tr_b16 v[236:237], v204 offset:0xc00
	v_mfma_f32_32x32x16_bf16 v[48:63], v[166:169], v[238:241], v[48:63]
	ds_read_b64_tr_b16 v[238:239], v204 offset:0x1400
	ds_read_b64_tr_b16 v[240:241], v204 offset:0x1c00
	v_mfma_f32_32x32x16_bf16 v[48:63], v[172:175], v[242:245], v[48:63]
	ds_read_b64_tr_b16 v[242:243], v204 offset:0x2400
	ds_read_b64_tr_b16 v[244:245], v204 offset:0x2c00
	v_mfma_f32_32x32x16_bf16 v[48:63], v[230:233], v[246:249], v[48:63]
	ds_read_b64_tr_b16 v[246:247], v204 offset:0x3400
	ds_read_b64_tr_b16 v[248:249], v204 offset:0x3c00
	s_waitcnt lgkmcnt(0)
	v_mfma_f32_32x32x16_bf16 v[32:47], v[162:165], v[234:237], v[32:47]
	ds_read_b64_tr_b16 v[234:235], v204 offset:0x600
	ds_read_b64_tr_b16 v[236:237], v204 offset:0xe00
	v_mfma_f32_32x32x16_bf16 v[32:47], v[166:169], v[238:241], v[32:47]
	ds_read_b64_tr_b16 v[238:239], v204 offset:0x1600
	ds_read_b64_tr_b16 v[240:241], v204 offset:0x1e00
	v_mfma_f32_32x32x16_bf16 v[32:47], v[172:175], v[242:245], v[32:47]
	ds_read_b64_tr_b16 v[242:243], v204 offset:0x2600
	ds_read_b64_tr_b16 v[244:245], v204 offset:0x2e00
	v_mfma_f32_32x32x16_bf16 v[32:47], v[230:233], v[246:249], v[32:47]
	ds_read_b64_tr_b16 v[246:247], v204 offset:0x3600
	ds_read_b64_tr_b16 v[248:249], v204 offset:0x3e00
	s_waitcnt lgkmcnt(0)
	v_mfma_f32_32x32x16_bf16 v[16:31], v[162:165], v[234:237], v[16:31]
	v_max_f32_e32 v162, v81, v81
	v_max_f32_e32 v163, v80, v80
	v_max_f32_e32 v162, v163, v162
	v_max3_f32 v162, v162, v82, v83
	v_max3_f32 v162, v162, v84, v85
	v_max3_f32 v162, v162, v86, v87
	v_max3_f32 v162, v162, v88, v89
	v_max3_f32 v162, v162, v90, v91
	v_max3_f32 v162, v162, v92, v93
	v_mfma_f32_32x32x16_bf16 v[16:31], v[166:169], v[238:241], v[16:31]
	v_max3_f32 v162, v162, v94, v95
	v_max3_f32 v162, v162, v64, v65
	v_max3_f32 v162, v162, v66, v67
	v_max3_f32 v162, v162, v68, v69
	v_max3_f32 v162, v162, v70, v71
	v_max3_f32 v162, v162, v72, v73
	v_max3_f32 v162, v162, v74, v75
	v_max3_f32 v162, v162, v76, v77
	v_mfma_f32_32x32x16_bf16 v[16:31], v[172:175], v[242:245], v[16:31]
	v_max3_f32 v162, v162, v78, v79
	v_mov_b32_e32 v163, v162
	s_nop 1
	v_permlane32_swap_b32_e32 v162, v163
	v_max_f32_e32 v163, v163, v163
	v_max_f32_e32 v162, v162, v162
	v_max_f32_e32 v162, v162, v163
	v_sub_f32_e32 v163, v162, v170
	v_cmp_ge_f32_e32 vcc, s87, v163
	v_max_f32_e32 v163, v170, v170
	v_max_f32_e32 v162, v163, v162
	v_mfma_f32_32x32x16_bf16 v[16:31], v[230:233], v[246:249], v[16:31]
	v_sub_f32_e32 v163, v170, v162
	v_mul_f32_e32 v163, 0x3e0293ee, v163
	v_exp_f32_e32 v163, v163
	s_cmp_eq_u64 vcc, exec
	s_cselect_b64 s[42:43], -1, 0
	s_waitcnt vmcnt(0)
	s_barrier
	v_cndmask_b32_e64 v229, v163, 1.0, s[42:43]
	v_cmp_gt_f32_e32 vcc, 1.0, v229
	s_cbranch_vccz .LBB0_429
	s_and_saveexec_b64 s[6:7], s[40:41]
	ds_write_b32 v201, v229 offset:128
	s_or_b64 exec, exec, s[6:7]
	s_waitcnt lgkmcnt(0)
	v_add_u32_e32 v163, v200, v96
	ds_read_b128 v[164:167], v163 offset:224
	ds_read_b128 v[172:175], v163 offset:192
	ds_read_b128 v[230:233], v163 offset:160
	ds_read_b128 v[234:237], v163 offset:128
	s_waitcnt lgkmcnt(3)
	v_pk_mul_f32 v[12:13], v[12:13], v[164:165]
	s_waitcnt lgkmcnt(2)
	v_pk_mul_f32 v[8:9], v[8:9], v[172:173]
	s_waitcnt lgkmcnt(1)
	v_pk_mul_f32 v[4:5], v[4:5], v[230:231]
	v_pk_mul_f32 v[14:15], v[14:15], v[166:167]
	v_pk_mul_f32 v[10:11], v[10:11], v[174:175]
	v_pk_mul_f32 v[6:7], v[6:7], v[232:233]
	s_waitcnt lgkmcnt(0)
	v_pk_mul_f32 v[2:3], v[2:3], v[236:237]
	v_pk_mul_f32 v[0:1], v[0:1], v[234:235]
	v_pk_mul_f32 v[60:61], v[60:61], v[164:165]
	v_pk_mul_f32 v[56:57], v[56:57], v[172:173]
	v_pk_mul_f32 v[52:53], v[52:53], v[230:231]
	v_pk_mul_f32 v[62:63], v[62:63], v[166:167]
	v_pk_mul_f32 v[58:59], v[58:59], v[174:175]
	v_pk_mul_f32 v[54:55], v[54:55], v[232:233]
	v_pk_mul_f32 v[50:51], v[50:51], v[236:237]
	v_pk_mul_f32 v[48:49], v[48:49], v[234:235]
	v_pk_mul_f32 v[44:45], v[44:45], v[164:165]
	v_pk_mul_f32 v[40:41], v[40:41], v[172:173]
	v_pk_mul_f32 v[36:37], v[36:37], v[230:231]
	v_pk_mul_f32 v[46:47], v[46:47], v[166:167]
	v_pk_mul_f32 v[42:43], v[42:43], v[174:175]
	v_pk_mul_f32 v[38:39], v[38:39], v[232:233]
	v_pk_mul_f32 v[34:35], v[34:35], v[236:237]
	v_pk_mul_f32 v[32:33], v[32:33], v[234:235]
	v_pk_mul_f32 v[28:29], v[28:29], v[164:165]
	v_pk_mul_f32 v[24:25], v[24:25], v[172:173]
	v_pk_mul_f32 v[20:21], v[20:21], v[230:231]
	v_pk_mul_f32 v[30:31], v[30:31], v[166:167]
	v_pk_mul_f32 v[26:27], v[26:27], v[174:175]
	v_pk_mul_f32 v[22:23], v[22:23], v[232:233]
	v_pk_mul_f32 v[18:19], v[18:19], v[236:237]
	v_pk_mul_f32 v[16:17], v[16:17], v[234:235]

; #define SBAR() __builtin_amdgcn_sched_barrier(0)
; __device__ __forceinline__ void partialSM(f32x16& p0, f32x16& p1, float& m_reg, float& mn, float& alpha) {
;     ...
;   float pmax = p0[0]; for (int r = 1; r < 16; ++r) pmax = fmaxf(pmax, p0[r]); for (int r = 0; r < 16; ++r) pmax = fmaxf(pmax, p1[r]);
;   { auto rr = __builtin_amdgcn_permlane32_swap(__float_as_uint(pmax), __float_as_uint(pmax), false, false);
;     pmax = fmaxf(__uint_as_float(rr[0]), __uint_as_float(rr[1])); }
;   if (__builtin_expect(__all(pmax - m_reg <= THR / SCALE), 1)) { mn = m_reg; alpha = 1.f; }
;   else { mn = fmaxf(m_reg, pmax); alpha = __builtin_amdgcn_exp2f((m_reg - mn) * C); m_reg = mn; }
; template <int D0> __device__ __forceinline__ void pv_one(f32x16& od, int vb, bf16x8 pa0, bf16x8 pa1, bf16x8 pa2, bf16x8 pa3) {
;   const s16x4 l0 = tr_read<v_rd_off(D0, 0, 0)>(vb), h0 = tr_read<v_rd_off(D0, 0, 1)>(vb), l1 = tr_read<v_rd_off(D0, 1, 0)>(vb), h1 = tr_read<v_rd_off(D0, 1, 1)>(vb);
;   const s16x4 l2 = tr_read<v_rd_off(D0, 2, 0)>(vb), h2 = tr_read<v_rd_off(D0, 2, 1)>(vb), l3 = tr_read<v_rd_off(D0, 3, 0)>(vb), h3 = tr_read<v_rd_off(D0, 3, 1)>(vb);
;   asm volatile("s_waitcnt lgkmcnt(0)" ::: "memory"); SBAR();
;     ...
;   od = __builtin_amdgcn_mfma_f32_32x32x16_bf16(pa0, PK(l0, h0), od, 0, 0, 0);
;   od = __builtin_amdgcn_mfma_f32_32x32x16_bf16(pa1, PK(l1, h1), od, 0, 0, 0);
;   od = __builtin_amdgcn_mfma_f32_32x32x16_bf16(pa2, PK(l2, h2), od, 0, 0, 0);
;   od = __builtin_amdgcn_mfma_f32_32x32x16_bf16(pa3, PK(l3, h3), od, 0, 0, 0);
;     ...
; }
; __device__ __forceinline__ void pv_d0(f32x16* o, int vb, bf16x8 pa0, bf16x8 pa1, bf16x8 pa2, bf16x8 pa3) {
;   pv_one<0>(o[0], vb, pa0, pa1, pa2, pa3); pv_one<1>(o[1], vb, pa0, pa1, pa2, pa3); pv_one<2>(o[2], vb, pa0, pa1, pa2, pa3); pv_one<3>(o[3], vb, pa0, pa1, pa2, pa3);
.LBB0_431:
	ds_read_b64_tr_b16 v[188:189], v203 offset:0
	ds_read_b64_tr_b16 v[190:191], v203 offset:0x800
	ds_read_b64_tr_b16 v[192:193], v203 offset:0x1000
	ds_read_b64_tr_b16 v[194:195], v203 offset:0x1800
	ds_read_b64_tr_b16 v[212:213], v203 offset:0x2000
	ds_read_b64_tr_b16 v[214:215], v203 offset:0x2800
	ds_read_b64_tr_b16 v[234:235], v203 offset:0x3000
	ds_read_b64_tr_b16 v[236:237], v203 offset:0x3800
	s_waitcnt lgkmcnt(0)
	s_nop 0
	v_mfma_f32_32x32x16_bf16 v[0:15], v[162:165], v[188:191], v[0:15]
	ds_read_b64_tr_b16 v[188:189], v203 offset:0x200
	ds_read_b64_tr_b16 v[190:191], v203 offset:0xa00
	v_mfma_f32_32x32x16_bf16 v[0:15], v[166:169], v[192:195], v[0:15]
	ds_read_b64_tr_b16 v[192:193], v203 offset:0x1200
	ds_read_b64_tr_b16 v[194:195], v203 offset:0x1a00
	v_mfma_f32_32x32x16_bf16 v[0:15], v[170:173], v[212:215], v[0:15]
	ds_read_b64_tr_b16 v[212:213], v203 offset:0x2200
	ds_read_b64_tr_b16 v[214:215], v203 offset:0x2a00
	v_mfma_f32_32x32x16_bf16 v[0:15], v[174:177], v[234:237], v[0:15]
	ds_read_b64_tr_b16 v[234:235], v203 offset:0x3200
	ds_read_b64_tr_b16 v[236:237], v203 offset:0x3a00
	s_waitcnt lgkmcnt(0)
	v_mfma_f32_32x32x16_bf16 v[48:63], v[162:165], v[188:191], v[48:63]
	ds_read_b64_tr_b16 v[188:189], v203 offset:0x400
	ds_read_b64_tr_b16 v[190:191], v203 offset:0xc00
	v_mfma_f32_32x32x16_bf16 v[48:63], v[166:169], v[192:195], v[48:63]
	ds_read_b64_tr_b16 v[192:193], v203 offset:0x1400
	ds_read_b64_tr_b16 v[194:195], v203 offset:0x1c00
	v_mfma_f32_32x32x16_bf16 v[48:63], v[170:173], v[212:215], v[48:63]
	ds_read_b64_tr_b16 v[212:213], v203 offset:0x2400
	ds_read_b64_tr_b16 v[214:215], v203 offset:0x2c00
	v_mfma_f32_32x32x16_bf16 v[48:63], v[174:177], v[234:237], v[48:63]
	ds_read_b64_tr_b16 v[234:235], v203 offset:0x3400
	ds_read_b64_tr_b16 v[236:237], v203 offset:0x3c00
	s_waitcnt lgkmcnt(0)
	v_mfma_f32_32x32x16_bf16 v[32:47], v[162:165], v[188:191], v[32:47]
	ds_read_b64_tr_b16 v[188:189], v203 offset:0x600
	ds_read_b64_tr_b16 v[190:191], v203 offset:0xe00
	v_mfma_f32_32x32x16_bf16 v[32:47], v[166:169], v[192:195], v[32:47]
	ds_read_b64_tr_b16 v[192:193], v203 offset:0x1600
	ds_read_b64_tr_b16 v[194:195], v203 offset:0x1e00
	v_mfma_f32_32x32x16_bf16 v[32:47], v[170:173], v[212:215], v[32:47]
	ds_read_b64_tr_b16 v[212:213], v203 offset:0x2600
	ds_read_b64_tr_b16 v[214:215], v203 offset:0x2e00
	v_mfma_f32_32x32x16_bf16 v[32:47], v[174:177], v[234:237], v[32:47]
	ds_read_b64_tr_b16 v[234:235], v203 offset:0x3600
	ds_read_b64_tr_b16 v[236:237], v203 offset:0x3e00
	s_waitcnt lgkmcnt(0)
	v_mfma_f32_32x32x16_bf16 v[16:31], v[162:165], v[188:191], v[16:31]
	v_max_f32_e32 v162, v81, v81
	v_max_f32_e32 v163, v80, v80
	v_max_f32_e32 v162, v163, v162
	v_max3_f32 v162, v162, v82, v83
	v_max3_f32 v162, v162, v84, v85
	v_max3_f32 v162, v162, v86, v87
	v_max3_f32 v162, v162, v88, v89
	v_max3_f32 v162, v162, v90, v91
	v_max3_f32 v162, v162, v92, v93
	v_mfma_f32_32x32x16_bf16 v[16:31], v[166:169], v[192:195], v[16:31]
	v_max3_f32 v162, v162, v94, v95
	v_max3_f32 v162, v162, v64, v65
	v_max3_f32 v162, v162, v66, v67
	v_max3_f32 v162, v162, v68, v69
	v_max3_f32 v162, v162, v70, v71
	v_max3_f32 v162, v162, v72, v73
	v_max3_f32 v162, v162, v74, v75
	v_max3_f32 v162, v162, v76, v77
	v_mfma_f32_32x32x16_bf16 v[16:31], v[170:173], v[212:215], v[16:31]
	v_max3_f32 v162, v162, v78, v79
	v_mov_b32_e32 v163, v162
	s_nop 1
	v_permlane32_swap_b32_e32 v162, v163
	v_max_f32_e32 v163, v163, v163
	v_max_f32_e32 v162, v162, v162
	v_max_f32_e32 v162, v162, v163
	v_sub_f32_e32 v163, v162, v230
	v_cmp_ge_f32_e32 vcc, s87, v163
	v_max_f32_e32 v163, v230, v230
	v_max_f32_e32 v163, v163, v162
	v_mfma_f32_32x32x16_bf16 v[16:31], v[174:177], v[234:237], v[16:31]
	v_sub_f32_e32 v162, v230, v163
	v_mul_f32_e32 v162, 0x3e0293ee, v162
	v_exp_f32_e32 v162, v162
	s_cmp_eq_u64 vcc, exec
	s_cselect_b64 s[42:43], -1, 0
	s_waitcnt vmcnt(0)
	s_barrier
	s_mov_b32 s54, 1
	v_cndmask_b32_e64 v162, v162, 1.0, s[42:43]
	v_cmp_gt_f32_e32 vcc, 1.0, v162
	s_cbranch_vccz .LBB0_435
	s_and_saveexec_b64 s[6:7], s[40:41]
	ds_write_b32 v201, v162 offset:128
	s_or_b64 exec, exec, s[6:7]
	s_waitcnt lgkmcnt(0)
	v_add_u32_e32 v158, v200, v96
	ds_read_b128 v[146:149], v158 offset:224
	ds_read_b128 v[150:153], v158 offset:192
	ds_read_b128 v[154:157], v158 offset:160
	ds_read_b128 v[158:161], v158 offset:128
	s_waitcnt lgkmcnt(3)
	v_pk_mul_f32 v[12:13], v[12:13], v[146:147]
	s_waitcnt lgkmcnt(2)
	v_pk_mul_f32 v[8:9], v[8:9], v[150:151]
	s_waitcnt lgkmcnt(1)
	v_pk_mul_f32 v[4:5], v[4:5], v[154:155]
	v_pk_mul_f32 v[14:15], v[14:15], v[148:149]
	v_pk_mul_f32 v[10:11], v[10:11], v[152:153]
	v_pk_mul_f32 v[6:7], v[6:7], v[156:157]
	s_waitcnt lgkmcnt(0)
	v_pk_mul_f32 v[2:3], v[2:3], v[160:161]
	v_pk_mul_f32 v[0:1], v[0:1], v[158:159]
	v_pk_mul_f32 v[60:61], v[60:61], v[146:147]
	v_pk_mul_f32 v[56:57], v[56:57], v[150:151]
	v_pk_mul_f32 v[52:53], v[52:53], v[154:155]
	v_pk_mul_f32 v[62:63], v[62:63], v[148:149]
	v_pk_mul_f32 v[58:59], v[58:59], v[152:153]
	v_pk_mul_f32 v[54:55], v[54:55], v[156:157]
	v_pk_mul_f32 v[50:51], v[50:51], v[160:161]
	v_pk_mul_f32 v[48:49], v[48:49], v[158:159]
	v_pk_mul_f32 v[44:45], v[44:45], v[146:147]
	v_pk_mul_f32 v[40:41], v[40:41], v[150:151]
	v_pk_mul_f32 v[36:37], v[36:37], v[154:155]
	v_pk_mul_f32 v[46:47], v[46:47], v[148:149]
	v_pk_mul_f32 v[42:43], v[42:43], v[152:153]
	v_pk_mul_f32 v[38:39], v[38:39], v[156:157]
	v_pk_mul_f32 v[34:35], v[34:35], v[160:161]
	v_pk_mul_f32 v[32:33], v[32:33], v[158:159]
	v_pk_mul_f32 v[28:29], v[28:29], v[146:147]
	v_pk_mul_f32 v[24:25], v[24:25], v[150:151]
	v_pk_mul_f32 v[20:21], v[20:21], v[154:155]
	v_pk_mul_f32 v[30:31], v[30:31], v[148:149]
	v_pk_mul_f32 v[26:27], v[26:27], v[152:153]
	v_pk_mul_f32 v[22:23], v[22:23], v[156:157]
	v_pk_mul_f32 v[18:19], v[18:19], v[160:161]
	v_pk_mul_f32 v[16:17], v[16:17], v[158:159]

; __device__ __forceinline__ void finishSM(f32x16& p0, f32x16& p1, float alpha, float& l_reg, bf16x8& pa0, bf16x8& pa1, bf16x8& pa2, bf16x8& pa3) {
;   for (int r = 0; r < 16; ++r) p1[r] = __builtin_amdgcn_exp2f(p1[r]);
;   float ps = 0; for (int r = 0; r < 16; ++r) ps += p0[r]; for (int r = 0; r < 16; ++r) ps += p1[r];
;   { auto rr = __builtin_amdgcn_permlane32_swap(__float_as_uint(ps), __float_as_uint(ps), false, false);
;     ps = __uint_as_float(rr[0]) + __uint_as_float(rr[1]); }
;   l_reg = l_reg * alpha + ps;
;     ...
;   PK4(p0, 0, pa0); PK4(p0, 8, pa1); PK4(p1, 0, pa2); PK4(p1, 8, pa3);
; template <bool HALF> __device__ __forceinline__ void qkt(f32x16& p0, f32x16& p1, const char* Ks, const bf16x8* qr, int r32, int hi, int koff) {
;   p0 = f32x16{}; p1 = f32x16{};
;   for (int d0 = 0; d0 < (HALF ? 4 : 8); ++d0) { int cb = (d0 * 16 + hi * 8) * 2 + koff;
;     bf16x8 b0 = *reinterpret_cast<const bf16x8*>(Ks + KSWZ(r32, cb));
;     bf16x8 b1 = *reinterpret_cast<const bf16x8*>(Ks + KSWZ(32 + r32, cb));
;     p0 = __builtin_amdgcn_mfma_f32_32x32x16_bf16(b0, qr[d0], p0, 0, 0, 0);
;     p1 = __builtin_amdgcn_mfma_f32_32x32x16_bf16(b1, qr[d0], p1, 0, 0, 0); }
.LBB0_437:
	ds_read_b128 v[64:67], v209 offset:49152
	ds_read_b128 v[68:71], v209 offset:57344
	s_waitcnt lgkmcnt(1)
	v_mfma_f32_32x32x16_bf16 v[80:95], v[64:67], v[118:121], 0
	s_waitcnt lgkmcnt(0)
	v_mfma_f32_32x32x16_bf16 v[64:79], v[68:71], v[118:121], 0
	ds_read_b128 v[118:121], v221 offset:49152
	ds_read_b128 v[130:133], v221 offset:57344
	s_waitcnt lgkmcnt(1)
	v_mfma_f32_32x32x16_bf16 v[80:95], v[118:121], v[126:129], v[80:95]
	s_add_i32 m0, s53, 0x4000
	s_nop 0
	global_load_lds_dwordx4 v140, s[50:51]
	s_add_i32 m0, s53, 0x4400
	s_nop 0
	global_load_lds_dwordx4 v141, s[50:51]
	s_waitcnt lgkmcnt(0)
	v_mfma_f32_32x32x16_bf16 v[64:79], v[130:133], v[126:129], v[64:79]
	ds_read_b128 v[118:121], v222 offset:49152
	ds_read_b128 v[126:129], v222 offset:57344
	s_waitcnt lgkmcnt(1)
	v_mfma_f32_32x32x16_bf16 v[80:95], v[118:121], v[122:125], v[80:95]
	s_waitcnt lgkmcnt(0)
	v_mfma_f32_32x32x16_bf16 v[64:79], v[126:129], v[122:125], v[64:79]
	ds_read_b128 v[118:121], v210 offset:49152
	ds_read_b128 v[122:125], v210 offset:57344
	s_waitcnt lgkmcnt(1)
	v_mfma_f32_32x32x16_bf16 v[80:95], v[118:121], v[114:117], v[80:95]
	s_waitcnt lgkmcnt(0)
	v_mfma_f32_32x32x16_bf16 v[64:79], v[122:125], v[114:117], v[64:79]
	ds_read_b128 v[114:117], v211 offset:49152
	ds_read_b128 v[118:121], v211 offset:57344
	v_exp_f32_e32 v122, v146
	v_exp_f32_e32 v123, v147
	s_waitcnt lgkmcnt(1)
	v_mfma_f32_32x32x16_bf16 v[80:95], v[114:117], v[110:113], v[80:95]
	s_waitcnt lgkmcnt(0)
	v_mfma_f32_32x32x16_bf16 v[64:79], v[118:121], v[110:113], v[64:79]
	ds_read_b128 v[110:113], v223 offset:49152
	ds_read_b128 v[114:117], v223 offset:57344
	v_exp_f32_e32 v118, v156
	v_exp_f32_e32 v119, v157
	v_exp_f32_e32 v120, v152
	v_exp_f32_e32 v121, v153
	s_waitcnt lgkmcnt(1)
	v_mfma_f32_32x32x16_bf16 v[80:95], v[110:113], v[106:109], v[80:95]
	s_waitcnt lgkmcnt(0)
	v_mfma_f32_32x32x16_bf16 v[64:79], v[114:117], v[106:109], v[64:79]
	ds_read_b128 v[106:109], v225 offset:49152
	ds_read_b128 v[110:113], v225 offset:57344
	v_exp_f32_e32 v114, v150
	v_exp_f32_e32 v115, v151
	v_exp_f32_e32 v116, v148
	v_exp_f32_e32 v117, v149
	s_waitcnt lgkmcnt(1)
	v_mfma_f32_32x32x16_bf16 v[80:95], v[106:109], v[102:105], v[80:95]
	s_waitcnt lgkmcnt(0)
	v_mfma_f32_32x32x16_bf16 v[64:79], v[110:113], v[102:105], v[64:79]
	ds_read_b128 v[102:105], v224 offset:49152
	ds_read_b128 v[106:109], v224 offset:57344
	v_exp_f32_e32 v110, v158
	v_exp_f32_e32 v111, v159
	v_exp_f32_e32 v112, v154
	v_exp_f32_e32 v113, v155
	s_waitcnt lgkmcnt(1)
	v_mfma_f32_32x32x16_bf16 v[80:95], v[102:105], v[98:101], v[80:95]
	s_waitcnt lgkmcnt(0)
	v_mfma_f32_32x32x16_bf16 v[64:79], v[106:109], v[98:101], v[64:79]
	v_add_f32_e32 v98, 0, v163
	v_add_f32_e32 v98, v177, v98
	v_add_f32_e32 v98, v164, v98
	v_add_f32_e32 v98, v188, v98
	v_add_f32_e32 v98, v176, v98
	v_add_f32_e32 v98, v189, v98
	v_add_f32_e32 v98, v165, v98
	v_add_f32_e32 v98, v175, v98
	v_add_f32_e32 v98, v166, v98
	v_add_f32_e32 v98, v173, v98
	v_add_f32_e32 v98, v167, v98
	v_add_f32_e32 v98, v174, v98
	v_exp_f32_e32 v108, v160
	v_add_f32_e32 v98, v168, v98
	v_exp_f32_e32 v109, v161
	v_add_f32_e32 v98, v171, v98
	v_add_f32_e32 v98, v169, v98
	v_add_f32_e32 v98, v172, v98
	v_add_f32_e32 v98, v108, v98
	v_add_f32_e32 v98, v109, v98
	v_add_f32_e32 v98, v110, v98
	v_add_f32_e32 v98, v111, v98
	v_add_f32_e32 v98, v112, v98
	v_add_f32_e32 v98, v113, v98
	v_add_f32_e32 v98, v114, v98
	v_add_f32_e32 v98, v115, v98
	v_add_f32_e32 v98, v116, v98
	v_add_f32_e32 v98, v117, v98
	v_add_f32_e32 v98, v118, v98
	v_add_f32_e32 v98, v119, v98
	v_add_f32_e32 v98, v120, v98
	v_add_f32_e32 v98, v121, v98
	v_add_f32_e32 v98, v122, v98
	v_add_f32_e32 v102, v123, v98
	v_mov_b32_e32 v103, v102
	v_cvt_pk_bf16_f32 v98, v163, v177
	v_cvt_pk_bf16_f32 v99, v164, v188
	v_cvt_pk_bf16_f32 v100, v176, v189
	v_cvt_pk_bf16_f32 v101, v165, v175
	s_nop 1
	v_permlane32_swap_b32_e32 v102, v103
	v_permlane32_swap_b32_e32 v98, v100
	v_permlane32_swap_b32_e32 v99, v101
	v_cvt_pk_bf16_f32 v104, v166, v173
	v_cvt_pk_bf16_f32 v105, v167, v174
	v_cvt_pk_bf16_f32 v106, v168, v171
	v_cvt_pk_bf16_f32 v107, v169, v172
	v_cvt_pk_bf16_f32 v108, v108, v109
	v_cvt_pk_bf16_f32 v109, v110, v111
	v_cvt_pk_bf16_f32 v110, v112, v113
	v_cvt_pk_bf16_f32 v111, v114, v115
	v_cvt_pk_bf16_f32 v112, v116, v117
	v_cvt_pk_bf16_f32 v113, v118, v119
	v_cvt_pk_bf16_f32 v114, v120, v121
	v_cvt_pk_bf16_f32 v115, v122, v123
	s_nop 0
	v_permlane32_swap_b32_e32 v104, v106
	v_permlane32_swap_b32_e32 v105, v107
	v_permlane32_swap_b32_e32 v108, v110
	v_permlane32_swap_b32_e32 v109, v111
	v_permlane32_swap_b32_e32 v112, v114
	v_permlane32_swap_b32_e32 v113, v115
	ds_read_b64_tr_b16 v[116:117], v204 offset:0
	ds_read_b64_tr_b16 v[118:119], v204 offset:0x800
	ds_read_b64_tr_b16 v[120:121], v204 offset:0x1000
	ds_read_b64_tr_b16 v[122:123], v204 offset:0x1800
	ds_read_b64_tr_b16 v[124:125], v204 offset:0x2000
	ds_read_b64_tr_b16 v[126:127], v204 offset:0x2800
	ds_read_b64_tr_b16 v[128:129], v204 offset:0x3000
	ds_read_b64_tr_b16 v[130:131], v204 offset:0x3800
	s_waitcnt lgkmcnt(0)
; #define SBAR() __builtin_amdgcn_sched_barrier(0)
; __device__ __forceinline__ void partialSM(f32x16& p0, f32x16& p1, float& m_reg, float& mn, float& alpha) {
;     ...
;   float pmax = p0[0]; for (int r = 1; r < 16; ++r) pmax = fmaxf(pmax, p0[r]); for (int r = 0; r < 16; ++r) pmax = fmaxf(pmax, p1[r]);
;   { auto rr = __builtin_amdgcn_permlane32_swap(__float_as_uint(pmax), __float_as_uint(pmax), false, false);
;     pmax = fmaxf(__uint_as_float(rr[0]), __uint_as_float(rr[1])); }
;   if (__builtin_expect(__all(pmax - m_reg <= THR / SCALE), 1)) { mn = m_reg; alpha = 1.f; }
;   else { mn = fmaxf(m_reg, pmax); alpha = __builtin_amdgcn_exp2f((m_reg - mn) * C); m_reg = mn; }
; template <int D0> __device__ __forceinline__ void pv_one(f32x16& od, int vb, bf16x8 pa0, bf16x8 pa1, bf16x8 pa2, bf16x8 pa3) {
;   const s16x4 l0 = tr_read<v_rd_off(D0, 0, 0)>(vb), h0 = tr_read<v_rd_off(D0, 0, 1)>(vb), l1 = tr_read<v_rd_off(D0, 1, 0)>(vb), h1 = tr_read<v_rd_off(D0, 1, 1)>(vb);
;   const s16x4 l2 = tr_read<v_rd_off(D0, 2, 0)>(vb), h2 = tr_read<v_rd_off(D0, 2, 1)>(vb), l3 = tr_read<v_rd_off(D0, 3, 0)>(vb), h3 = tr_read<v_rd_off(D0, 3, 1)>(vb);
;   asm volatile("s_waitcnt lgkmcnt(0)" ::: "memory"); SBAR();
;     ...
;   od = __builtin_amdgcn_mfma_f32_32x32x16_bf16(pa0, PK(l0, h0), od, 0, 0, 0);
;   od = __builtin_amdgcn_mfma_f32_32x32x16_bf16(pa1, PK(l1, h1), od, 0, 0, 0);
;   od = __builtin_amdgcn_mfma_f32_32x32x16_bf16(pa2, PK(l2, h2), od, 0, 0, 0);
;   od = __builtin_amdgcn_mfma_f32_32x32x16_bf16(pa3, PK(l3, h3), od, 0, 0, 0);
;     ...
; }
; __device__ __forceinline__ void pv_d0(f32x16* o, int vb, bf16x8 pa0, bf16x8 pa1, bf16x8 pa2, bf16x8 pa3) {
;   pv_one<0>(o[0], vb, pa0, pa1, pa2, pa3); pv_one<1>(o[1], vb, pa0, pa1, pa2, pa3); pv_one<2>(o[2], vb, pa0, pa1, pa2, pa3); pv_one<3>(o[3], vb, pa0, pa1, pa2, pa3);
	s_nop 0
	v_mfma_f32_32x32x16_bf16 v[0:15], v[98:101], v[116:119], v[0:15]
	ds_read_b64_tr_b16 v[116:117], v204 offset:0x200
	ds_read_b64_tr_b16 v[118:119], v204 offset:0xa00
	v_mfma_f32_32x32x16_bf16 v[0:15], v[104:107], v[120:123], v[0:15]
	ds_read_b64_tr_b16 v[120:121], v204 offset:0x1200
	ds_read_b64_tr_b16 v[122:123], v204 offset:0x1a00
	v_mfma_f32_32x32x16_bf16 v[0:15], v[108:111], v[124:127], v[0:15]
	ds_read_b64_tr_b16 v[124:125], v204 offset:0x2200
	ds_read_b64_tr_b16 v[126:127], v204 offset:0x2a00
	v_mfma_f32_32x32x16_bf16 v[0:15], v[112:115], v[128:131], v[0:15]
	ds_read_b64_tr_b16 v[128:129], v204 offset:0x3200
	ds_read_b64_tr_b16 v[130:131], v204 offset:0x3a00
	s_waitcnt lgkmcnt(0)
	v_mfma_f32_32x32x16_bf16 v[48:63], v[98:101], v[116:119], v[48:63]
	ds_read_b64_tr_b16 v[116:117], v204 offset:0x400
	ds_read_b64_tr_b16 v[118:119], v204 offset:0xc00
	v_mfma_f32_32x32x16_bf16 v[48:63], v[104:107], v[120:123], v[48:63]
	ds_read_b64_tr_b16 v[120:121], v204 offset:0x1400
	ds_read_b64_tr_b16 v[122:123], v204 offset:0x1c00
	v_mfma_f32_32x32x16_bf16 v[48:63], v[108:111], v[124:127], v[48:63]
	ds_read_b64_tr_b16 v[124:125], v204 offset:0x2400
	ds_read_b64_tr_b16 v[126:127], v204 offset:0x2c00
	v_mfma_f32_32x32x16_bf16 v[48:63], v[112:115], v[128:131], v[48:63]
	ds_read_b64_tr_b16 v[128:129], v204 offset:0x3400
	ds_read_b64_tr_b16 v[130:131], v204 offset:0x3c00
	s_waitcnt lgkmcnt(0)
	v_mfma_f32_32x32x16_bf16 v[32:47], v[98:101], v[116:119], v[32:47]
	ds_read_b64_tr_b16 v[116:117], v204 offset:0x600
	ds_read_b64_tr_b16 v[118:119], v204 offset:0xe00
	v_mfma_f32_32x32x16_bf16 v[32:47], v[104:107], v[120:123], v[32:47]
	ds_read_b64_tr_b16 v[120:121], v204 offset:0x1600
	ds_read_b64_tr_b16 v[122:123], v204 offset:0x1e00
	v_mfma_f32_32x32x16_bf16 v[32:47], v[108:111], v[124:127], v[32:47]
	ds_read_b64_tr_b16 v[124:125], v204 offset:0x2600
	ds_read_b64_tr_b16 v[126:127], v204 offset:0x2e00
	v_mfma_f32_32x32x16_bf16 v[32:47], v[112:115], v[128:131], v[32:47]
	ds_read_b64_tr_b16 v[128:129], v204 offset:0x3600
	ds_read_b64_tr_b16 v[130:131], v204 offset:0x3e00
	s_waitcnt lgkmcnt(0)
	v_mfma_f32_32x32x16_bf16 v[16:31], v[98:101], v[116:119], v[16:31]
	v_max_f32_e32 v98, v81, v81
	v_max_f32_e32 v99, v80, v80
	v_max_f32_e32 v98, v99, v98
	v_max3_f32 v98, v98, v82, v83
	v_max3_f32 v98, v98, v84, v85
	v_max3_f32 v98, v98, v86, v87
	v_max3_f32 v98, v98, v88, v89
	v_max3_f32 v98, v98, v90, v91
	v_max3_f32 v98, v98, v92, v93
	v_mfma_f32_32x32x16_bf16 v[16:31], v[104:107], v[120:123], v[16:31]
	v_max3_f32 v98, v98, v94, v95
	v_max3_f32 v98, v98, v64, v65
	v_max3_f32 v98, v98, v66, v67
	v_max3_f32 v98, v98, v68, v69
	v_max3_f32 v98, v98, v70, v71
	v_max3_f32 v98, v98, v72, v73
	v_max3_f32 v98, v98, v74, v75
	v_max3_f32 v98, v98, v76, v77
	v_mfma_f32_32x32x16_bf16 v[16:31], v[108:111], v[124:127], v[16:31]
	v_max3_f32 v98, v98, v78, v79
	v_mov_b32_e32 v99, v98
	s_nop 1
	v_permlane32_swap_b32_e32 v98, v99
	v_max_f32_e32 v99, v99, v99
	v_max_f32_e32 v98, v98, v98
	v_max_f32_e32 v98, v98, v99
	v_sub_f32_e32 v99, v98, v170
	v_cmp_ge_f32_e32 vcc, s87, v99
	v_max_f32_e32 v99, v170, v170
	v_max_f32_e32 v99, v99, v98
	v_mfma_f32_32x32x16_bf16 v[16:31], v[112:115], v[128:131], v[16:31]
	v_sub_f32_e32 v98, v170, v99
	v_mul_f32_e32 v98, 0x3e0293ee, v98
	v_exp_f32_e32 v98, v98
	s_cmp_eq_u64 vcc, exec
	s_cselect_b64 s[42:43], -1, 0
	v_cndmask_b32_e64 v98, v98, 1.0, s[42:43]
	v_cmp_gt_f32_e32 vcc, 1.0, v98
	s_waitcnt vmcnt(0)
	s_barrier
	s_cbranch_vccz .LBB0_441
	s_and_saveexec_b64 s[6:7], s[40:41]
	ds_write_b32 v201, v98 offset:128
	s_or_b64 exec, exec, s[6:7]
	s_waitcnt lgkmcnt(0)
	v_add_u32_e32 v100, v200, v96
	ds_read_b128 v[104:107], v100 offset:224
	ds_read_b128 v[108:111], v100 offset:192
	ds_read_b128 v[112:115], v100 offset:160
	ds_read_b128 v[116:119], v100 offset:128
	s_waitcnt lgkmcnt(3)
	v_pk_mul_f32 v[12:13], v[12:13], v[104:105]
	s_waitcnt lgkmcnt(2)
	v_pk_mul_f32 v[8:9], v[8:9], v[108:109]
	s_waitcnt lgkmcnt(1)
	v_pk_mul_f32 v[4:5], v[4:5], v[112:113]
	v_pk_mul_f32 v[14:15], v[14:15], v[106:107]
	v_pk_mul_f32 v[10:11], v[10:11], v[110:111]
	v_pk_mul_f32 v[6:7], v[6:7], v[114:115]
	s_waitcnt lgkmcnt(0)
	v_pk_mul_f32 v[2:3], v[2:3], v[118:119]
	v_pk_mul_f32 v[0:1], v[0:1], v[116:117]
	v_pk_mul_f32 v[60:61], v[60:61], v[104:105]
	v_pk_mul_f32 v[56:57], v[56:57], v[108:109]
	v_pk_mul_f32 v[52:53], v[52:53], v[112:113]
	v_pk_mul_f32 v[62:63], v[62:63], v[106:107]
	v_pk_mul_f32 v[58:59], v[58:59], v[110:111]
	v_pk_mul_f32 v[54:55], v[54:55], v[114:115]
	v_pk_mul_f32 v[50:51], v[50:51], v[118:119]
	v_pk_mul_f32 v[48:49], v[48:49], v[116:117]
	v_pk_mul_f32 v[44:45], v[44:45], v[104:105]
	v_pk_mul_f32 v[40:41], v[40:41], v[108:109]
	v_pk_mul_f32 v[36:37], v[36:37], v[112:113]
	v_pk_mul_f32 v[46:47], v[46:47], v[106:107]
	v_pk_mul_f32 v[42:43], v[42:43], v[110:111]
	v_pk_mul_f32 v[38:39], v[38:39], v[114:115]
	v_pk_mul_f32 v[34:35], v[34:35], v[118:119]
	v_pk_mul_f32 v[32:33], v[32:33], v[116:117]
	v_pk_mul_f32 v[28:29], v[28:29], v[104:105]
	v_pk_mul_f32 v[24:25], v[24:25], v[108:109]
	v_pk_mul_f32 v[20:21], v[20:21], v[112:113]
	v_pk_mul_f32 v[30:31], v[30:31], v[106:107]
	v_pk_mul_f32 v[26:27], v[26:27], v[110:111]
	v_pk_mul_f32 v[22:23], v[22:23], v[114:115]
	v_pk_mul_f32 v[18:19], v[18:19], v[118:119]
	v_pk_mul_f32 v[16:17], v[16:17], v[116:117]

; __device__ __forceinline__ unsigned cvtpk(float lo, float hi) { unsigned r; asm volatile("v_cvt_pk_bf16_f32 %0, %1, %2" : "=v"(r) : "v"(lo), "v"(hi)); return r; }
; __device__ __forceinline__ int v_st(int k, int c) { const int kk = (k & ~0xC) | ((k & 4) << 1) | ((k & 8) >> 1); return ((kk >> 3) * 4 + (c >> 5)) * 512 + ((kk & 7) * 32 + (c & 31)) * 2; }
; template <bool HALF> __device__ __forceinline__ void dense_body(const bf16_t* __restrict__ Qb, const bf16_t* __restrict__ Kh, const bf16_t* __restrict__ Vh, ...
;     ...
; #pragma unroll
;     for (int d0 = 0; d0 < NQ; ++d0) { u32x4 w;
; #pragma unroll
;       for (int j = 0; j < 4; ++j) w[j] = cvtpk(qf[d0][2 * j], qf[d0][2 * j + 1]);
;       qr[d0] = *reinterpret_cast<bf16x8*>(&w); } }
;   const int sr = tid >> 4, sc = (tid & 15) * 8, vst0 = v_st(sr, sc), vst1 = v_st(32 + sr, sc);
;   const int vb0 = (int)(uintptr_t)V_lds + v_rd_base(lane);
;   struct { bf16x8 vs0, vs1, ks0, ks1; } sr_[2];
;   const unsigned ko0 = (unsigned)(sr * LDKK + sc) * 2u, ko1 = ko0 + 32u * LDKK * 2u, vo0 = (unsigned)(sr * LDKV + sc) * 2u, vo1 = vo0 + 32u * LDKV * 2u;
;     ...
;   f32x16 pA0, pA1, pB0, pB1; float mnA, mnB, alA, alB; bf16x8 pa0, pa1, pa2, pa3; const int NT = seq / KVBLK;
;   const char* Kl0 = (const char*)K_lds; const char* Kl1 = (const char*)(K_lds + SHM_K);
;   constexpr int SE = 0, SO = 1;
;   SLOAD(SE, 0); asm volatile("s_waitcnt vmcnt(0)" ::: "memory"); SWRITE(0, SE); __syncthreads();
;   qkt<HALF>(pA0, pA1, Kl0, qr, r32, hi, koff); partialSM(pA0, pA1, m_reg, mnA, alA);
;   SLOAD(SO, KVBLK); if (2 < NT) SLOAD(SE, 2 * KVBLK);
; template <bool HALF> __device__ __forceinline__ void unit(const P& p, int l, int u, LAS char* lds, int tid) {
;     ...
;   if (u < 512) { hq = ((u >> 8) << 3) + (u & 7); qrow = CTXL + ((u >> 3) & 31) * 256; nk = NTOK; } else { hq = u - 512; qrow = 0; nk = CTXL; }
;   const int kvh = hq < 8 ? (hq >> 2) : 2 + ((hq - 8) >> 1);
;   const bf16_t* Qb = WSP(bf16_t, WS_PROJ) + (size_t)qrow * INW + (hq < 8 ? C_AQ + hq * 128 : C_DQ + (hq - 8) * 64);
;   const bf16_t* Kh = WSP(bf16_t, WS_KALL) + kvh * 128;
;   const bf16_t* Vh = WSP(bf16_t, WS_PROJ) + (kvh < 2 ? C_AV + kvh * 128 : C_DV + (kvh - 2) * 128);
;   bf16_t* Obf = !HALF ? WSP(bf16_t, WS_MIX) + (size_t)qrow * DM + 512 + hq * 128 : nullptr;
;   float* Of = !HALF ? nullptr : WSP(float, WS_DTMP) + (size_t)qrow * 1024 + (hq - 8) * 128;
.LBB0_453:
	s_ashr_i32 s18, s3, 2
	s_add_i32 s3, s3, -8
	s_lshr_b32 s3, s3, 1
	s_add_i32 s3, s3, 2
	s_and_b64 s[6:7], s[14:15], exec
	s_cselect_b32 s3, s18, s3
	s_lshl_b32 s6, s3, 7
	s_cmp_lt_i32 s3, 2
	s_movk_i32 s3, 0x1100
	s_cselect_b32 s3, s3, 0x1500
	s_ashr_i32 s7, s6, 31
	s_add_i32 s18, s3, s6
	s_lshl_b64 s[14:15], s[6:7], 1
	v_cvt_pk_bf16_f32 v98, v30, v20
	v_cvt_pk_bf16_f32 v99, v31, v21
	v_cvt_pk_bf16_f32 v100, v32, v18
	v_cvt_pk_bf16_f32 v101, v33, v19
	v_cvt_pk_bf16_f32 v106, v34, v16
	v_cvt_pk_bf16_f32 v107, v35, v17
	v_ashrrev_i32_e32 v16, 4, v44
	v_lshlrev_b32_e32 v17, 3, v44
	s_movk_i32 s3, 0x300
	s_add_u32 s20, s44, s14
	v_and_b32_e32 v18, 0x78, v17
	v_mul_lo_u32 v0, v16, s3
	s_addc_u32 s21, s45, s15
	s_ashr_i32 s19, s18, 31
	v_or_b32_e32 v0, v0, v18
	s_movk_i32 s3, 0x1800
	s_lshl_b64 s[18:19], s[18:19], 1
	v_lshlrev_b32_e32 v50, 1, v0
	v_mul_lo_u32 v0, v16, s3
	s_add_u32 s22, s30, s18
	v_or_b32_e32 v0, v0, v18
	s_addc_u32 s23, s31, s19
	v_lshlrev_b32_e32 v54, 1, v0
	v_cvt_pk_bf16_f32 v108, v40, v10
	v_cvt_pk_bf16_f32 v109, v41, v11
	v_cvt_pk_bf16_f32 v110, v4, v8
	v_cvt_pk_bf16_f32 v111, v5, v9
	v_cvt_pk_bf16_f32 v112, v2, v36
	v_cvt_pk_bf16_f32 v113, v1, v37
	v_cvt_pk_bf16_f32 v102, v24, v6
	v_cvt_pk_bf16_f32 v103, v23, v7
	v_cvt_pk_bf16_f32 v104, v14, v26
	v_cvt_pk_bf16_f32 v105, v13, v27
	v_add_u32_e32 v48, 0xc000, v50
	v_add_u32_e32 v52, 0x60000, v54
	v_readlane_b32 s52, v252, 4
	s_nop 3
	v_and_b32_e32 v236, 63, v44
	v_lshrrev_b32_e32 v237, 4, v236
	v_and_b32_e32 v238, 15, v236
	s_lshl_b32 s53, s52, 3
	v_add_u32_e32 v239, s53, v237
	v_xor_b32_e32 v240, v238, v237
	v_mul_u32_u24_e32 v232, 0x600, v239
	v_lshl_add_u32 v232, v240, 4, v232
	v_add_u32_e32 v241, 4, v237
	v_xor_b32_e32 v240, v238, v241
	v_add_u32_e32 v239, 4, v239
	v_mul_u32_u24_e32 v233, 0x600, v239
	v_lshl_add_u32 v233, v240, 4, v233
	v_bfe_u32 v237, v236, 2, 3
	v_add_u32_e32 v237, s53, v237
	v_and_b32_e32 v238, 4, v237
	v_and_b32_e32 v239, 8, v237
	v_and_b32_e32 v237, 0xfffffff3, v237
	v_lshl_or_b32 v237, v238, 1, v237
	v_lshrrev_b32_e32 v239, 1, v239
	v_or_b32_e32 v237, v237, v239
	v_mul_u32_u24_e32 v234, 0x3000, v237
	v_lshrrev_b32_e32 v238, 5, v236
	v_lshl_add_u32 v234, v238, 6, v234
	v_and_b32_e32 v238, 3, v236
	v_lshl_add_u32 v234, v238, 4, v234
	v_add_u32_e32 v235, 0x80, v234
	s_lshl_b32 s53, s52, 11
	s_add_i32 s52, s53, 0x8000
	s_add_i32 m0, s52, 0x0
	s_nop 0
	global_load_lds_dwordx4 v232, s[20:21]
	s_add_i32 m0, s52, 0x400
	s_nop 0
	global_load_lds_dwordx4 v233, s[20:21]
	s_add_i32 m0, s53, 0x0
	s_nop 0
	global_load_lds_dwordx4 v234, s[22:23]
	s_add_i32 m0, s53, 0x400
	s_nop 0
	global_load_lds_dwordx4 v235, s[22:23]
	s_add_u32 s48, s20, 0x18000
	s_addc_u32 s49, s21, 0
	s_add_u32 s50, s22, 0xc0000
	s_addc_u32 s51, s23, 0
	s_add_i32 m0, s52, 0x4000
	s_nop 0
	global_load_lds_dwordx4 v232, s[48:49]
	s_add_i32 m0, s52, 0x4400
	s_nop 0
	global_load_lds_dwordx4 v233, s[48:49]
	s_add_i32 m0, s53, 0x4000
	s_nop 0
	global_load_lds_dwordx4 v234, s[50:51]
	s_add_i32 m0, s53, 0x4400
	s_nop 0
	global_load_lds_dwordx4 v235, s[50:51]
	s_add_u32 s48, s48, 0x18000
	s_addc_u32 s49, s49, 0
	s_add_u32 s50, s50, 0xc0000
	s_addc_u32 s51, s51, 0
	v_lshlrev_b32_e32 v20, 4, v180
	v_and_b32_e32 v21, 0xfffff0, v16
	v_lshlrev_b32_e32 v22, 1, v16
	v_lshrrev_b32_e32 v23, 1, v16
	v_and_b32_e32 v24, 3, v16
	v_add_u32_e32 v25, 32, v16
	v_and_b32_e32 v73, 0x70, v20
	v_and_or_b32 v20, v22, 8, v21
	v_and_b32_e32 v19, 0x70, v44
	v_bfe_u32 v17, v17, 5, 2
	v_lshlrev_b32_e32 v16, 8, v16
	v_and_or_b32 v21, v23, 4, v24
	v_lshlrev_b32_e32 v18, 1, v18
	v_and_b32_e32 v22, 0xfffff0, v25
	v_lshlrev_b32_e32 v23, 1, v25
	v_lshlrev_b32_e32 v24, 8, v25
	v_lshrrev_b32_e32 v20, 1, v20
	v_and_b32_e32 v25, 48, v18
	v_and_or_b32 v22, v23, 8, v22
	v_bitop3_b32 v16, v18, v16, v19 bitop3:0xde
	v_bitop3_b32 v18, v18, v24, v19 bitop3:0xde
	v_or_b32_e32 v19, v20, v17
	v_lshlrev_b32_e32 v21, 6, v21
	v_lshrrev_b32_e32 v20, 1, v22
	v_add_u32_e32 v188, 0, v16
	v_lshlrev_b32_e32 v16, 9, v19
	s_and_b32 s3, s17, 0x80
	v_lshlrev_b32_e32 v72, 8, v180
	v_or_b32_e32 v17, v20, v17
	v_or3_b32 v16, v16, v21, v25
	v_or_b32_e32 v74, s3, v96
	v_lshlrev_b32_e32 v17, 9, v17
	v_add_u32_e32 v190, 0, v16
	v_bitop3_b32 v16, v74, v72, v73 bitop3:0xde
	v_or3_b32 v17, v17, v21, v25
	v_add_u32_e32 v192, 0, v16
	v_add_u32_e32 v189, 0, v18
	v_add_u32_e32 v191, 0, v17
	s_waitcnt vmcnt(0)
	v_and_b32_e32 v76, 63, v44
	s_add_u32 s6, s20, 0x18000
	s_addc_u32 s7, s21, 0
	s_add_u32 s38, s22, 0xc0000
	s_addc_u32 s39, s23, 0
	s_mov_b32 s64, s65
	s_waitcnt lgkmcnt(0)
	s_barrier
; __device__ __forceinline__ void partialSM(f32x16& p0, f32x16& p1, float& m_reg, float& mn, float& alpha) {
;   constexpr float C = SCALE * 1.4426950408889634f;
;   float pmax = p0[0]; for (int r = 1; r < 16; ++r) pmax = fmaxf(pmax, p0[r]); for (int r = 0; r < 16; ++r) pmax = fmaxf(pmax, p1[r]);
;   { auto rr = __builtin_amdgcn_permlane32_swap(__float_as_uint(pmax), __float_as_uint(pmax), false, false);
;     pmax = fmaxf(__uint_as_float(rr[0]), __uint_as_float(rr[1])); }
;   if (__builtin_expect(__all(pmax - m_reg <= THR / SCALE), 1)) { mn = m_reg; alpha = 1.f; }
;   else { mn = fmaxf(m_reg, pmax); alpha = __builtin_amdgcn_exp2f((m_reg - mn) * C); m_reg = mn; }
;   float mnC = -mn * C;
;   for (int r = 0; r < 16; ++r) p0[r] = fmaf(p0[r], C, mnC); for (int r = 0; r < 16; ++r) p1[r] = fmaf(p1[r], C, mnC);
;   for (int r = 0; r < 16; ++r) p0[r] = __builtin_amdgcn_exp2f(p0[r]);
; }
; template <bool HALF> __device__ __forceinline__ void qkt(f32x16& p0, f32x16& p1, const char* Ks, const bf16x8* qr, int r32, int hi, int koff) {
;   p0 = f32x16{}; p1 = f32x16{};
;   for (int d0 = 0; d0 < (HALF ? 4 : 8); ++d0) { int cb = (d0 * 16 + hi * 8) * 2 + koff;
;     bf16x8 b0 = *reinterpret_cast<const bf16x8*>(Ks + KSWZ(r32, cb));
;     bf16x8 b1 = *reinterpret_cast<const bf16x8*>(Ks + KSWZ(32 + r32, cb));
;     p0 = __builtin_amdgcn_mfma_f32_32x32x16_bf16(b0, qr[d0], p0, 0, 0, 0);
;     p1 = __builtin_amdgcn_mfma_f32_32x32x16_bf16(b1, qr[d0], p1, 0, 0, 0); }
	ds_read_b128 v[0:3], v192 offset:32768
	ds_read_b128 v[4:7], v192 offset:40960
	s_waitcnt lgkmcnt(1)
	v_mfma_f32_32x32x16_bf16 v[16:31], v[0:3], v[98:101], 0
	v_and_b32_e32 v0, 0x3fffffc0, v44
	v_lshl_add_u32 v183, v0, 2, s46
	v_lshlrev_b32_e32 v0, 4, v76
	v_lshlrev_b32_e32 v8, 3, v76
	v_and_b32_e32 v0, 0xc0, v0
	v_and_or_b32 v9, v8, 24, v0
	v_or_b32_e32 v0, 32, v74
	v_bitop3_b32 v0, v0, v72, v73 bitop3:0xde
	v_add_u32_e32 v193, 0, v0
	s_waitcnt lgkmcnt(0)
	v_mfma_f32_32x32x16_bf16 v[32:47], v[4:7], v[98:101], 0
	ds_read_b128 v[0:3], v193 offset:32768
	ds_read_b128 v[4:7], v193 offset:40960
	s_add_u32 s6, s20, 0x30000
	s_addc_u32 s7, s21, 0
	v_and_b32_e32 v8, 0x100, v8
	s_mov_b32 s66, s65
	s_mov_b32 s67, s65
	s_waitcnt lgkmcnt(1)
	v_mfma_f32_32x32x16_bf16 v[16:31], v[0:3], v[106:109], v[16:31]
	v_lshlrev_b32_e32 v0, 1, v76
	v_and_b32_e32 v10, 32, v0
	v_or_b32_e32 v0, 64, v74
	v_bitop3_b32 v0, v0, v72, v73 bitop3:0xde
	v_add_u32_e32 v195, 0, v0
	ds_read_b128 v[0:3], v195 offset:32768
	v_or3_b32 v77, v9, v10, v8
	s_waitcnt lgkmcnt(1)
	v_mfma_f32_32x32x16_bf16 v[32:47], v[4:7], v[106:109], v[32:47]
	ds_read_b128 v[4:7], v195 offset:40960
	s_mov_b32 s68, s65
	s_mov_b32 s69, s65
	s_mov_b32 s70, s65
	s_mov_b32 s71, s65
	s_mov_b32 s72, s65
	s_mov_b32 s73, s65
	s_waitcnt lgkmcnt(1)
	v_mfma_f32_32x32x16_bf16 v[16:31], v[0:3], v[110:113], v[16:31]
	v_or_b32_e32 v0, 0x60, v74
	v_bitop3_b32 v0, v0, v72, v73 bitop3:0xde
	v_add_u32_e32 v194, 0, v0
	ds_read_b128 v[0:3], v194 offset:32768
	ds_read_b128 v[72:75], v194 offset:40960
	s_add_u32 s6, s22, 0x180000
	s_addc_u32 s7, s23, 0
	s_waitcnt lgkmcnt(2)
	v_mfma_f32_32x32x16_bf16 v[32:47], v[4:7], v[110:113], v[32:47]
	s_mov_b32 s74, s65
	s_mov_b32 s75, s65
	s_waitcnt lgkmcnt(1)
	v_mfma_f32_32x32x16_bf16 v[16:31], v[0:3], v[102:105], v[16:31]
	s_mov_b32 s76, s65
	s_mov_b32 s77, s65
	s_mov_b32 s78, s65
	s_mov_b32 s79, s65
	v_mov_b64_e32 v[0:1], s[64:65]
	v_mov_b32_e32 v55, v97
	v_mov_b32_e32 v53, v97
	s_waitcnt lgkmcnt(0)
	v_mfma_f32_32x32x16_bf16 v[32:47], v[72:75], v[102:105], v[32:47]
	s_nop 2
	v_max_f32_e32 v72, v17, v17
	v_max_f32_e32 v73, v16, v16
	v_max_f32_e32 v72, v73, v72
	v_max3_f32 v72, v72, v18, v19
	v_max3_f32 v72, v72, v20, v21
	v_max3_f32 v72, v72, v22, v23
	v_max3_f32 v72, v72, v24, v25
	v_max3_f32 v72, v72, v26, v27
	v_max3_f32 v72, v72, v28, v29
	v_max3_f32 v72, v72, v30, v31
	v_max3_f32 v72, v72, v32, v33
	v_max3_f32 v72, v72, v34, v35
	v_max3_f32 v72, v72, v36, v37
	v_max3_f32 v72, v72, v38, v39
	v_max3_f32 v72, v72, v40, v41
	v_max3_f32 v72, v72, v42, v43
	v_max3_f32 v72, v72, v44, v45
	v_max3_f32 v72, v72, v46, v47
	v_mov_b32_e32 v73, v72
	s_nop 1
	v_permlane32_swap_b32_e32 v72, v73
	v_max_f32_e32 v73, v73, v73
	v_max_f32_e32 v72, v72, v72
	v_max_f32_e32 v72, v72, v73
	v_add_f32_e32 v73, 0x7149f2ca, v72
	v_cmp_ge_f32_e32 vcc, s87, v73
	s_cmp_eq_u64 vcc, exec
	v_max_f32_e32 v56, 0xf149f2ca, v72
	s_cselect_b64 vcc, -1, 0
	v_cndmask_b32_e32 v150, v56, v217, vcc
	v_sub_f32_e32 v57, 0xf149f2ca, v56
	v_mul_f32_e32 v56, 0xbe0293ee, v150
	v_fmamk_f32 v16, v16, 0x3e0293ee, v56
	v_exp_f32_e32 v147, v16
	v_fmamk_f32 v16, v17, 0x3e0293ee, v56
	v_exp_f32_e32 v160, v16
	v_fmamk_f32 v16, v18, 0x3e0293ee, v56
	v_exp_f32_e32 v148, v16
	v_fmamk_f32 v16, v19, 0x3e0293ee, v56
	v_exp_f32_e32 v161, v16
	v_fmamk_f32 v16, v20, 0x3e0293ee, v56
	v_exp_f32_e32 v149, v16
	v_fmamk_f32 v16, v21, 0x3e0293ee, v56
	v_exp_f32_e32 v170, v16
	v_fmamk_f32 v16, v22, 0x3e0293ee, v56
	v_exp_f32_e32 v159, v16
	v_fmamk_f32 v16, v23, 0x3e0293ee, v56
	v_exp_f32_e32 v171, v16
	v_fmamk_f32 v16, v24, 0x3e0293ee, v56
	v_mul_f32_e32 v57, 0x3e0293ee, v57
	v_exp_f32_e32 v151, v16
	v_fmamk_f32 v16, v25, 0x3e0293ee, v56
	v_exp_f32_e32 v57, v57
	v_exp_f32_e32 v155, v16
	v_fmamk_f32 v16, v26, 0x3e0293ee, v56
	v_exp_f32_e32 v152, v16
	v_fmamk_f32 v16, v27, 0x3e0293ee, v56
	v_exp_f32_e32 v156, v16
	v_fmamk_f32 v16, v28, 0x3e0293ee, v56
	v_exp_f32_e32 v153, v16
	v_fmamk_f32 v16, v29, 0x3e0293ee, v56
	v_pk_fma_f32 v[130:131], v[46:47], s[10:11], v[56:57] op_sel_hi:[1,0,0]
	v_pk_fma_f32 v[136:137], v[44:45], s[10:11], v[56:57] op_sel_hi:[1,0,0]
	v_pk_fma_f32 v[140:141], v[42:43], s[10:11], v[56:57] op_sel_hi:[1,0,0]
	v_pk_fma_f32 v[132:133], v[40:41], s[10:11], v[56:57] op_sel_hi:[1,0,0]
	v_pk_fma_f32 v[134:135], v[38:39], s[10:11], v[56:57] op_sel_hi:[1,0,0]
	v_pk_fma_f32 v[138:139], v[36:37], s[10:11], v[56:57] op_sel_hi:[1,0,0]
	v_pk_fma_f32 v[142:143], v[34:35], s[10:11], v[56:57] op_sel_hi:[1,0,0]
	v_pk_fma_f32 v[144:145], v[32:33], s[10:11], v[56:57] op_sel_hi:[1,0,0]
	v_exp_f32_e32 v157, v16
	v_fmamk_f32 v16, v30, 0x3e0293ee, v56
	v_fmac_f32_e32 v56, 0x3e0293ee, v31
	v_exp_f32_e32 v154, v16
	v_exp_f32_e32 v158, v56
	v_mov_b32_e32 v51, v97
	v_mov_b32_e32 v49, v97
	v_mov_b64_e32 v[14:15], s[78:79]
	v_mov_b64_e32 v[2:3], s[66:67]
	v_mov_b64_e32 v[4:5], s[68:69]
	v_mov_b64_e32 v[6:7], s[70:71]
	v_mov_b64_e32 v[8:9], s[72:73]
	v_mov_b64_e32 v[10:11], s[74:75]
	v_mov_b64_e32 v[12:13], s[76:77]
	v_cndmask_b32_e64 v197, v57, 1.0, vcc
	v_lshl_add_u64 v[162:163], s[18:19], 0, v[54:55]
	v_lshl_add_u64 v[164:165], s[18:19], 0, v[52:53]
	v_lshl_add_u64 v[166:167], s[14:15], 0, v[50:51]
	v_lshl_add_u64 v[168:169], s[14:15], 0, v[48:49]
	v_mov_b64_e32 v[62:63], v[14:15]
	v_mov_b64_e32 v[46:47], v[14:15]
	v_mov_b64_e32 v[30:31], v[14:15]
	s_mov_b32 s3, 4
	v_add_u32_e32 v187, 0, v77
	v_cmp_gt_u32_e64 s[40:41], 32, v76
	v_lshl_add_u32 v184, v180, 2, v183
	v_add_u32_e32 v186, s34, v77
	v_mov_b32_e32 v185, 0
	v_mov_b64_e32 v[60:61], v[12:13]
	v_mov_b64_e32 v[58:59], v[10:11]
	v_mov_b64_e32 v[56:57], v[8:9]
	v_mov_b64_e32 v[54:55], v[6:7]
	v_mov_b64_e32 v[52:53], v[4:5]
	v_mov_b64_e32 v[50:51], v[2:3]
	v_mov_b64_e32 v[48:49], v[0:1]
	v_mov_b64_e32 v[44:45], v[12:13]
	v_mov_b64_e32 v[42:43], v[10:11]
	v_mov_b64_e32 v[40:41], v[8:9]
	v_mov_b64_e32 v[38:39], v[6:7]
	v_mov_b64_e32 v[36:37], v[4:5]
	v_mov_b64_e32 v[34:35], v[2:3]
	v_mov_b64_e32 v[32:33], v[0:1]
	v_mov_b64_e32 v[28:29], v[12:13]
	v_mov_b64_e32 v[26:27], v[10:11]
	v_mov_b64_e32 v[24:25], v[8:9]
	v_mov_b64_e32 v[22:23], v[6:7]
	v_mov_b64_e32 v[20:21], v[4:5]
	v_mov_b64_e32 v[18:19], v[2:3]
	v_mov_b64_e32 v[16:17], v[0:1]
	v_readlane_b32 s78, v255, 23
	s_waitcnt lgkmcnt(0)
	s_barrier
	v_readlane_b32 s79, v255, 24
	s_add_i32 m0, s52, 0x0
	s_nop 0
	global_load_lds_dwordx4 v232, s[48:49]
	s_add_i32 m0, s52, 0x400
	s_nop 0
	global_load_lds_dwordx4 v233, s[48:49]
	s_add_u32 s48, s48, 0x18000
	s_addc_u32 s49, s49, 0
	s_mov_b32 s54, 0
; __device__ __forceinline__ void finishSM(f32x16& p0, f32x16& p1, float alpha, float& l_reg, bf16x8& pa0, bf16x8& pa1, bf16x8& pa2, bf16x8& pa3) {
;   for (int r = 0; r < 16; ++r) p1[r] = __builtin_amdgcn_exp2f(p1[r]);
;   float ps = 0; for (int r = 0; r < 16; ++r) ps += p0[r]; for (int r = 0; r < 16; ++r) ps += p1[r];
;   { auto rr = __builtin_amdgcn_permlane32_swap(__float_as_uint(ps), __float_as_uint(ps), false, false);
;     ps = __uint_as_float(rr[0]) + __uint_as_float(rr[1]); }
;   l_reg = l_reg * alpha + ps;
;     ...
;   PK4(p0, 0, pa0); PK4(p0, 8, pa1); PK4(p1, 0, pa2); PK4(p1, 8, pa3);
; template <bool HALF> __device__ __forceinline__ void qkt(f32x16& p0, f32x16& p1, const char* Ks, const bf16x8* qr, int r32, int hi, int koff) {
;   p0 = f32x16{}; p1 = f32x16{};
;   for (int d0 = 0; d0 < (HALF ? 4 : 8); ++d0) { int cb = (d0 * 16 + hi * 8) * 2 + koff;
;     bf16x8 b0 = *reinterpret_cast<const bf16x8*>(Ks + KSWZ(r32, cb));
;     bf16x8 b1 = *reinterpret_cast<const bf16x8*>(Ks + KSWZ(32 + r32, cb));
;     p0 = __builtin_amdgcn_mfma_f32_32x32x16_bf16(b0, qr[d0], p0, 0, 0, 0);
;     p1 = __builtin_amdgcn_mfma_f32_32x32x16_bf16(b1, qr[d0], p1, 0, 0, 0); }
.LBB0_454:
	ds_read_b128 v[64:67], v192 offset:49152
	ds_read_b128 v[68:71], v192 offset:57344
	v_add_f32_e32 v146, 0, v147
	v_add_f32_e32 v146, v160, v146
	v_add_f32_e32 v146, v148, v146
	s_waitcnt lgkmcnt(1)
	v_mfma_f32_32x32x16_bf16 v[80:95], v[64:67], v[98:101], 0
	v_add_f32_e32 v146, v161, v146
	v_add_f32_e32 v146, v149, v146
	ds_read_b128 v[172:175], v193 offset:49152
	ds_read_b128 v[198:201], v193 offset:57344
	v_add_f32_e32 v146, v170, v146
	v_add_f32_e32 v146, v159, v146
	v_add_f32_e32 v146, v171, v146
	v_add_f32_e32 v146, v151, v146
	s_waitcnt lgkmcnt(2)
	v_mfma_f32_32x32x16_bf16 v[64:79], v[68:71], v[98:101], 0
	v_add_f32_e32 v146, v155, v146
	v_add_f32_e32 v146, v152, v146
	v_add_f32_e32 v146, v156, v146
	v_exp_f32_e32 v144, v144
	v_add_f32_e32 v146, v153, v146
	v_exp_f32_e32 v145, v145
	v_add_f32_e32 v146, v157, v146
	s_waitcnt lgkmcnt(1)
	v_mfma_f32_32x32x16_bf16 v[80:95], v[172:175], v[106:109], v[80:95]
	s_cmp_eq_u32 s54, 0
	s_cbranch_scc1 .Lmv_h
	s_add_i32 m0, s52, 0x0
	s_nop 0
	global_load_lds_dwordx4 v232, s[48:49]
	s_add_i32 m0, s52, 0x400
	s_nop 0
	global_load_lds_dwordx4 v233, s[48:49]
	s_add_u32 s48, s48, 0x18000
	s_addc_u32 s49, s49, 0
	s_add_i32 m0, s53, 0x4000
	s_nop 0
	global_load_lds_dwordx4 v234, s[50:51]
	s_add_i32 m0, s53, 0x4400
	s_nop 0
	global_load_lds_dwordx4 v235, s[50:51]
	s_add_u32 s50, s50, 0xc0000
	s_addc_u32 s51, s51, 0
.Lmv_h:
	v_exp_f32_e32 v142, v142
	v_add_f32_e32 v146, v154, v146
	v_exp_f32_e32 v143, v143
	v_add_f32_e32 v146, v158, v146
	v_exp_f32_e32 v138, v138
	v_add_f32_e32 v146, v144, v146
	v_exp_f32_e32 v139, v139
	s_waitcnt lgkmcnt(0)
	v_mfma_f32_32x32x16_bf16 v[64:79], v[198:201], v[106:109], v[64:79]
	ds_read_b128 v[172:175], v195 offset:49152
	ds_read_b128 v[198:201], v195 offset:57344
	v_add_f32_e32 v146, v145, v146
	v_exp_f32_e32 v134, v134
	v_add_f32_e32 v146, v142, v146
	v_exp_f32_e32 v135, v135
	v_add_f32_e32 v146, v143, v146
	v_exp_f32_e32 v132, v132
	s_waitcnt lgkmcnt(1)
	v_mfma_f32_32x32x16_bf16 v[80:95], v[172:175], v[110:113], v[80:95]
	v_add_f32_e32 v146, v138, v146
	v_exp_f32_e32 v133, v133
	v_add_f32_e32 v146, v139, v146
	v_exp_f32_e32 v140, v140
	v_add_f32_e32 v146, v134, v146
	v_exp_f32_e32 v141, v141
	v_add_f32_e32 v146, v135, v146
	s_waitcnt lgkmcnt(0)
	v_mfma_f32_32x32x16_bf16 v[64:79], v[198:201], v[110:113], v[64:79]
	ds_read_b128 v[172:175], v194 offset:49152
	ds_read_b128 v[198:201], v194 offset:57344
	v_exp_f32_e32 v136, v136
	v_add_f32_e32 v146, v132, v146
	v_exp_f32_e32 v137, v137
	v_add_f32_e32 v146, v133, v146
	v_exp_f32_e32 v130, v130
	v_add_f32_e32 v146, v140, v146
	s_waitcnt lgkmcnt(1)
	v_mfma_f32_32x32x16_bf16 v[80:95], v[172:175], v[102:105], v[80:95]
	v_exp_f32_e32 v131, v131
	v_add_f32_e32 v146, v141, v146
	v_add_f32_e32 v146, v136, v146
	v_add_f32_e32 v146, v137, v146
	v_add_f32_e32 v146, v130, v146
	s_waitcnt lgkmcnt(0)
	v_mfma_f32_32x32x16_bf16 v[64:79], v[198:201], v[102:105], v[64:79]
	v_add_f32_e32 v198, v131, v146
	v_mov_b32_e32 v199, v198
	v_cvt_pk_bf16_f32 v146, v147, v160
	v_cvt_pk_bf16_f32 v147, v148, v161
	v_cvt_pk_bf16_f32 v148, v149, v170
	v_cvt_pk_bf16_f32 v149, v159, v171
	v_cvt_pk_bf16_f32 v200, v151, v155
	v_cvt_pk_bf16_f32 v201, v152, v156
	v_cvt_pk_bf16_f32 v202, v153, v157
	s_nop 1
	v_permlane32_swap_b32_e32 v198, v199
	v_permlane32_swap_b32_e32 v146, v148
	v_cvt_pk_bf16_f32 v203, v154, v158
	v_permlane32_swap_b32_e32 v200, v202
	v_cvt_pk_bf16_f32 v152, v144, v145
	v_cvt_pk_bf16_f32 v153, v142, v143
	v_cvt_pk_bf16_f32 v154, v138, v139
	v_cvt_pk_bf16_f32 v155, v134, v135
	v_cvt_pk_bf16_f32 v156, v132, v133
	v_cvt_pk_bf16_f32 v157, v140, v141
	v_cvt_pk_bf16_f32 v158, v136, v137
	v_cvt_pk_bf16_f32 v159, v130, v131
	v_permlane32_swap_b32_e32 v147, v149
	v_permlane32_swap_b32_e32 v201, v203
	v_permlane32_swap_b32_e32 v152, v154
	v_permlane32_swap_b32_e32 v153, v155
	v_permlane32_swap_b32_e32 v156, v158
	v_permlane32_swap_b32_e32 v157, v159
	ds_read_b64_tr_b16 v[204:205], v187 offset:0
	ds_read_b64_tr_b16 v[206:207], v187 offset:0x800
	ds_read_b64_tr_b16 v[208:209], v187 offset:0x1000
	ds_read_b64_tr_b16 v[210:211], v187 offset:0x1800
	ds_read_b64_tr_b16 v[212:213], v187 offset:0x2000
	ds_read_b64_tr_b16 v[214:215], v187 offset:0x2800
	ds_read_b64_tr_b16 v[222:223], v187 offset:0x3000
	ds_read_b64_tr_b16 v[224:225], v187 offset:0x3800
	s_waitcnt lgkmcnt(0)
	s_nop 0
	v_mfma_f32_32x32x16_bf16 v[0:15], v[146:149], v[204:207], v[0:15]
	ds_read_b64_tr_b16 v[204:205], v187 offset:0x200
	ds_read_b64_tr_b16 v[206:207], v187 offset:0xa00
	v_mfma_f32_32x32x16_bf16 v[0:15], v[200:203], v[208:211], v[0:15]
	ds_read_b64_tr_b16 v[208:209], v187 offset:0x1200
	ds_read_b64_tr_b16 v[210:211], v187 offset:0x1a00
	v_mfma_f32_32x32x16_bf16 v[0:15], v[152:155], v[212:215], v[0:15]
	ds_read_b64_tr_b16 v[212:213], v187 offset:0x2200
	ds_read_b64_tr_b16 v[214:215], v187 offset:0x2a00
	v_mfma_f32_32x32x16_bf16 v[0:15], v[156:159], v[222:225], v[0:15]
	ds_read_b64_tr_b16 v[222:223], v187 offset:0x3200
	ds_read_b64_tr_b16 v[224:225], v187 offset:0x3a00
	s_waitcnt lgkmcnt(0)
; #define SBAR() __builtin_amdgcn_sched_barrier(0)
; __device__ __forceinline__ void partialSM(f32x16& p0, f32x16& p1, float& m_reg, float& mn, float& alpha) {
;     ...
;   float pmax = p0[0]; for (int r = 1; r < 16; ++r) pmax = fmaxf(pmax, p0[r]); for (int r = 0; r < 16; ++r) pmax = fmaxf(pmax, p1[r]);
;   { auto rr = __builtin_amdgcn_permlane32_swap(__float_as_uint(pmax), __float_as_uint(pmax), false, false);
;     pmax = fmaxf(__uint_as_float(rr[0]), __uint_as_float(rr[1])); }
;   if (__builtin_expect(__all(pmax - m_reg <= THR / SCALE), 1)) { mn = m_reg; alpha = 1.f; }
;   else { mn = fmaxf(m_reg, pmax); alpha = __builtin_amdgcn_exp2f((m_reg - mn) * C); m_reg = mn; }
; template <int D0> __device__ __forceinline__ void pv_one(f32x16& od, int vb, bf16x8 pa0, bf16x8 pa1, bf16x8 pa2, bf16x8 pa3) {
;   const s16x4 l0 = tr_read<v_rd_off(D0, 0, 0)>(vb), h0 = tr_read<v_rd_off(D0, 0, 1)>(vb), l1 = tr_read<v_rd_off(D0, 1, 0)>(vb), h1 = tr_read<v_rd_off(D0, 1, 1)>(vb);
;   const s16x4 l2 = tr_read<v_rd_off(D0, 2, 0)>(vb), h2 = tr_read<v_rd_off(D0, 2, 1)>(vb), l3 = tr_read<v_rd_off(D0, 3, 0)>(vb), h3 = tr_read<v_rd_off(D0, 3, 1)>(vb);
;   asm volatile("s_waitcnt lgkmcnt(0)" ::: "memory"); SBAR();
;     ...
;   od = __builtin_amdgcn_mfma_f32_32x32x16_bf16(pa0, PK(l0, h0), od, 0, 0, 0);
;   od = __builtin_amdgcn_mfma_f32_32x32x16_bf16(pa1, PK(l1, h1), od, 0, 0, 0);
;   od = __builtin_amdgcn_mfma_f32_32x32x16_bf16(pa2, PK(l2, h2), od, 0, 0, 0);
;   od = __builtin_amdgcn_mfma_f32_32x32x16_bf16(pa3, PK(l3, h3), od, 0, 0, 0);
;     ...
; }
; __device__ __forceinline__ void pv_d0(f32x16* o, int vb, bf16x8 pa0, bf16x8 pa1, bf16x8 pa2, bf16x8 pa3) {
;   pv_one<0>(o[0], vb, pa0, pa1, pa2, pa3); pv_one<1>(o[1], vb, pa0, pa1, pa2, pa3); pv_one<2>(o[2], vb, pa0, pa1, pa2, pa3); pv_one<3>(o[3], vb, pa0, pa1, pa2, pa3);
	v_mfma_f32_32x32x16_bf16 v[48:63], v[146:149], v[204:207], v[48:63]
	ds_read_b64_tr_b16 v[204:205], v187 offset:0x400
	ds_read_b64_tr_b16 v[206:207], v187 offset:0xc00
	v_mfma_f32_32x32x16_bf16 v[48:63], v[200:203], v[208:211], v[48:63]
	ds_read_b64_tr_b16 v[208:209], v187 offset:0x1400
	ds_read_b64_tr_b16 v[210:211], v187 offset:0x1c00
	v_mfma_f32_32x32x16_bf16 v[48:63], v[152:155], v[212:215], v[48:63]
	ds_read_b64_tr_b16 v[212:213], v187 offset:0x2400
	ds_read_b64_tr_b16 v[214:215], v187 offset:0x2c00
	v_mfma_f32_32x32x16_bf16 v[48:63], v[156:159], v[222:225], v[48:63]
	ds_read_b64_tr_b16 v[222:223], v187 offset:0x3400
	ds_read_b64_tr_b16 v[224:225], v187 offset:0x3c00
	s_waitcnt lgkmcnt(0)
	v_mfma_f32_32x32x16_bf16 v[32:47], v[146:149], v[204:207], v[32:47]
	ds_read_b64_tr_b16 v[204:205], v187 offset:0x600
	ds_read_b64_tr_b16 v[206:207], v187 offset:0xe00
	v_mfma_f32_32x32x16_bf16 v[32:47], v[200:203], v[208:211], v[32:47]
	ds_read_b64_tr_b16 v[208:209], v187 offset:0x1600
	ds_read_b64_tr_b16 v[210:211], v187 offset:0x1e00
	v_mfma_f32_32x32x16_bf16 v[32:47], v[152:155], v[212:215], v[32:47]
	ds_read_b64_tr_b16 v[212:213], v187 offset:0x2600
	ds_read_b64_tr_b16 v[214:215], v187 offset:0x2e00
	v_mfma_f32_32x32x16_bf16 v[32:47], v[156:159], v[222:225], v[32:47]
	ds_read_b64_tr_b16 v[222:223], v187 offset:0x3600
	ds_read_b64_tr_b16 v[224:225], v187 offset:0x3e00
	s_waitcnt lgkmcnt(0)
	v_mfma_f32_32x32x16_bf16 v[16:31], v[146:149], v[204:207], v[16:31]
	v_max_f32_e32 v146, v81, v81
	v_max_f32_e32 v147, v80, v80
	v_max_f32_e32 v146, v147, v146
	v_max3_f32 v146, v146, v82, v83
	v_max3_f32 v146, v146, v84, v85
	v_max3_f32 v146, v146, v86, v87
	v_max3_f32 v146, v146, v88, v89
	v_max3_f32 v146, v146, v90, v91
	v_max3_f32 v146, v146, v92, v93
	v_mfma_f32_32x32x16_bf16 v[16:31], v[200:203], v[208:211], v[16:31]
	v_max3_f32 v146, v146, v94, v95
	v_max3_f32 v146, v146, v64, v65
	v_max3_f32 v146, v146, v66, v67
	v_max3_f32 v146, v146, v68, v69
	v_max3_f32 v146, v146, v70, v71
	v_max3_f32 v146, v146, v72, v73
	v_max3_f32 v146, v146, v74, v75
	v_max3_f32 v146, v146, v76, v77
	v_mfma_f32_32x32x16_bf16 v[16:31], v[152:155], v[212:215], v[16:31]
	v_max3_f32 v146, v146, v78, v79
	v_mov_b32_e32 v147, v146
	s_nop 1
	v_permlane32_swap_b32_e32 v146, v147
	v_max_f32_e32 v147, v147, v147
	v_max_f32_e32 v146, v146, v146
	v_max_f32_e32 v146, v146, v147
	v_sub_f32_e32 v147, v146, v150
	v_cmp_ge_f32_e32 vcc, s87, v147
	v_max_f32_e32 v147, v150, v150
	v_max_f32_e32 v146, v147, v146
	v_mfma_f32_32x32x16_bf16 v[16:31], v[156:159], v[222:225], v[16:31]
	v_sub_f32_e32 v147, v150, v146
	v_mul_f32_e32 v147, 0x3e0293ee, v147
	v_exp_f32_e32 v147, v147
	s_cmp_eq_u64 vcc, exec
	s_cselect_b64 s[42:43], -1, 0
	s_waitcnt vmcnt(0)
	s_barrier
	v_cndmask_b32_e64 v200, v147, 1.0, s[42:43]
	v_cmp_gt_f32_e32 vcc, 1.0, v200
	s_cbranch_vccz .LBB0_458
	s_and_saveexec_b64 s[6:7], s[40:41]
	ds_write_b32 v184, v200 offset:128
	s_or_b64 exec, exec, s[6:7]
	s_waitcnt lgkmcnt(0)
	v_add_u32_e32 v147, v183, v96
	ds_read_b128 v[152:155], v147 offset:224
	ds_read_b128 v[156:159], v147 offset:192
	ds_read_b128 v[202:205], v147 offset:160
	ds_read_b128 v[206:209], v147 offset:128
	s_waitcnt lgkmcnt(3)
	v_pk_mul_f32 v[12:13], v[12:13], v[152:153]
	s_waitcnt lgkmcnt(2)
	v_pk_mul_f32 v[8:9], v[8:9], v[156:157]
	s_waitcnt lgkmcnt(1)
	v_pk_mul_f32 v[4:5], v[4:5], v[202:203]
	v_pk_mul_f32 v[14:15], v[14:15], v[154:155]
	v_pk_mul_f32 v[10:11], v[10:11], v[158:159]
	v_pk_mul_f32 v[6:7], v[6:7], v[204:205]
	s_waitcnt lgkmcnt(0)
	v_pk_mul_f32 v[2:3], v[2:3], v[208:209]
	v_pk_mul_f32 v[0:1], v[0:1], v[206:207]
	v_pk_mul_f32 v[60:61], v[60:61], v[152:153]
	v_pk_mul_f32 v[56:57], v[56:57], v[156:157]
	v_pk_mul_f32 v[52:53], v[52:53], v[202:203]
	v_pk_mul_f32 v[62:63], v[62:63], v[154:155]
	v_pk_mul_f32 v[58:59], v[58:59], v[158:159]
	v_pk_mul_f32 v[54:55], v[54:55], v[204:205]
	v_pk_mul_f32 v[50:51], v[50:51], v[208:209]
	v_pk_mul_f32 v[48:49], v[48:49], v[206:207]
	v_pk_mul_f32 v[44:45], v[44:45], v[152:153]
	v_pk_mul_f32 v[40:41], v[40:41], v[156:157]
	v_pk_mul_f32 v[36:37], v[36:37], v[202:203]
	v_pk_mul_f32 v[46:47], v[46:47], v[154:155]
	v_pk_mul_f32 v[42:43], v[42:43], v[158:159]
	v_pk_mul_f32 v[38:39], v[38:39], v[204:205]
	v_pk_mul_f32 v[34:35], v[34:35], v[208:209]
	v_pk_mul_f32 v[32:33], v[32:33], v[206:207]
	v_pk_mul_f32 v[28:29], v[28:29], v[152:153]
	v_pk_mul_f32 v[24:25], v[24:25], v[156:157]
	v_pk_mul_f32 v[20:21], v[20:21], v[202:203]
	v_pk_mul_f32 v[30:31], v[30:31], v[154:155]
	v_pk_mul_f32 v[26:27], v[26:27], v[158:159]
	v_pk_mul_f32 v[22:23], v[22:23], v[204:205]
	v_pk_mul_f32 v[18:19], v[18:19], v[208:209]
	v_pk_mul_f32 v[16:17], v[16:17], v[206:207]

; #define SBAR() __builtin_amdgcn_sched_barrier(0)
; __device__ __forceinline__ void partialSM(f32x16& p0, f32x16& p1, float& m_reg, float& mn, float& alpha) {
;     ...
;   float pmax = p0[0]; for (int r = 1; r < 16; ++r) pmax = fmaxf(pmax, p0[r]); for (int r = 0; r < 16; ++r) pmax = fmaxf(pmax, p1[r]);
;   { auto rr = __builtin_amdgcn_permlane32_swap(__float_as_uint(pmax), __float_as_uint(pmax), false, false);
;     pmax = fmaxf(__uint_as_float(rr[0]), __uint_as_float(rr[1])); }
;   if (__builtin_expect(__all(pmax - m_reg <= THR / SCALE), 1)) { mn = m_reg; alpha = 1.f; }
;   else { mn = fmaxf(m_reg, pmax); alpha = __builtin_amdgcn_exp2f((m_reg - mn) * C); m_reg = mn; }
; template <int D0> __device__ __forceinline__ void pv_one(f32x16& od, int vb, bf16x8 pa0, bf16x8 pa1, bf16x8 pa2, bf16x8 pa3) {
;   const s16x4 l0 = tr_read<v_rd_off(D0, 0, 0)>(vb), h0 = tr_read<v_rd_off(D0, 0, 1)>(vb), l1 = tr_read<v_rd_off(D0, 1, 0)>(vb), h1 = tr_read<v_rd_off(D0, 1, 1)>(vb);
;   const s16x4 l2 = tr_read<v_rd_off(D0, 2, 0)>(vb), h2 = tr_read<v_rd_off(D0, 2, 1)>(vb), l3 = tr_read<v_rd_off(D0, 3, 0)>(vb), h3 = tr_read<v_rd_off(D0, 3, 1)>(vb);
;   asm volatile("s_waitcnt lgkmcnt(0)" ::: "memory"); SBAR();
;     ...
;   od = __builtin_amdgcn_mfma_f32_32x32x16_bf16(pa0, PK(l0, h0), od, 0, 0, 0);
;   od = __builtin_amdgcn_mfma_f32_32x32x16_bf16(pa1, PK(l1, h1), od, 0, 0, 0);
;   od = __builtin_amdgcn_mfma_f32_32x32x16_bf16(pa2, PK(l2, h2), od, 0, 0, 0);
;   od = __builtin_amdgcn_mfma_f32_32x32x16_bf16(pa3, PK(l3, h3), od, 0, 0, 0);
;     ...
; }
; __device__ __forceinline__ void pv_d0(f32x16* o, int vb, bf16x8 pa0, bf16x8 pa1, bf16x8 pa2, bf16x8 pa3) {
;   pv_one<0>(o[0], vb, pa0, pa1, pa2, pa3); pv_one<1>(o[1], vb, pa0, pa1, pa2, pa3); pv_one<2>(o[2], vb, pa0, pa1, pa2, pa3); pv_one<3>(o[3], vb, pa0, pa1, pa2, pa3);
.LBB0_460:
	ds_read_b64_tr_b16 v[170:171], v186 offset:0
	ds_read_b64_tr_b16 v[172:173], v186 offset:0x800
	ds_read_b64_tr_b16 v[174:175], v186 offset:0x1000
	ds_read_b64_tr_b16 v[176:177], v186 offset:0x1800
	ds_read_b64_tr_b16 v[204:205], v186 offset:0x2000
	ds_read_b64_tr_b16 v[206:207], v186 offset:0x2800
	ds_read_b64_tr_b16 v[208:209], v186 offset:0x3000
	ds_read_b64_tr_b16 v[210:211], v186 offset:0x3800
	s_waitcnt lgkmcnt(0)
	s_nop 0
	v_mfma_f32_32x32x16_bf16 v[0:15], v[146:149], v[170:173], v[0:15]
	ds_read_b64_tr_b16 v[170:171], v186 offset:0x200
	ds_read_b64_tr_b16 v[172:173], v186 offset:0xa00
	v_mfma_f32_32x32x16_bf16 v[0:15], v[150:153], v[174:177], v[0:15]
	ds_read_b64_tr_b16 v[174:175], v186 offset:0x1200
	ds_read_b64_tr_b16 v[176:177], v186 offset:0x1a00
	v_mfma_f32_32x32x16_bf16 v[0:15], v[154:157], v[204:207], v[0:15]
	ds_read_b64_tr_b16 v[204:205], v186 offset:0x2200
	ds_read_b64_tr_b16 v[206:207], v186 offset:0x2a00
	v_mfma_f32_32x32x16_bf16 v[0:15], v[158:161], v[208:211], v[0:15]
	ds_read_b64_tr_b16 v[208:209], v186 offset:0x3200
	ds_read_b64_tr_b16 v[210:211], v186 offset:0x3a00
	s_waitcnt lgkmcnt(0)
	v_mfma_f32_32x32x16_bf16 v[48:63], v[146:149], v[170:173], v[48:63]
	ds_read_b64_tr_b16 v[170:171], v186 offset:0x400
	ds_read_b64_tr_b16 v[172:173], v186 offset:0xc00
	v_mfma_f32_32x32x16_bf16 v[48:63], v[150:153], v[174:177], v[48:63]
	ds_read_b64_tr_b16 v[174:175], v186 offset:0x1400
	ds_read_b64_tr_b16 v[176:177], v186 offset:0x1c00
	v_mfma_f32_32x32x16_bf16 v[48:63], v[154:157], v[204:207], v[48:63]
	ds_read_b64_tr_b16 v[204:205], v186 offset:0x2400
	ds_read_b64_tr_b16 v[206:207], v186 offset:0x2c00
	v_mfma_f32_32x32x16_bf16 v[48:63], v[158:161], v[208:211], v[48:63]
	ds_read_b64_tr_b16 v[208:209], v186 offset:0x3400
	ds_read_b64_tr_b16 v[210:211], v186 offset:0x3c00
	s_waitcnt lgkmcnt(0)
	v_mfma_f32_32x32x16_bf16 v[32:47], v[146:149], v[170:173], v[32:47]
	ds_read_b64_tr_b16 v[170:171], v186 offset:0x600
	ds_read_b64_tr_b16 v[172:173], v186 offset:0xe00
	v_mfma_f32_32x32x16_bf16 v[32:47], v[150:153], v[174:177], v[32:47]
	ds_read_b64_tr_b16 v[174:175], v186 offset:0x1600
	ds_read_b64_tr_b16 v[176:177], v186 offset:0x1e00
	v_mfma_f32_32x32x16_bf16 v[32:47], v[154:157], v[204:207], v[32:47]
	ds_read_b64_tr_b16 v[204:205], v186 offset:0x2600
	ds_read_b64_tr_b16 v[206:207], v186 offset:0x2e00
	v_mfma_f32_32x32x16_bf16 v[32:47], v[158:161], v[208:211], v[32:47]
	ds_read_b64_tr_b16 v[208:209], v186 offset:0x3600
	ds_read_b64_tr_b16 v[210:211], v186 offset:0x3e00
	s_waitcnt lgkmcnt(0)
	v_mfma_f32_32x32x16_bf16 v[16:31], v[146:149], v[170:173], v[16:31]
	v_max_f32_e32 v146, v81, v81
	v_max_f32_e32 v147, v80, v80
	v_max_f32_e32 v146, v147, v146
	v_max3_f32 v146, v146, v82, v83
	v_max3_f32 v146, v146, v84, v85
	v_max3_f32 v146, v146, v86, v87
	v_max3_f32 v146, v146, v88, v89
	v_max3_f32 v146, v146, v90, v91
	v_max3_f32 v146, v146, v92, v93
	v_mfma_f32_32x32x16_bf16 v[16:31], v[150:153], v[174:177], v[16:31]
	v_max3_f32 v146, v146, v94, v95
	v_max3_f32 v146, v146, v64, v65
	v_max3_f32 v146, v146, v66, v67
	v_max3_f32 v146, v146, v68, v69
	v_max3_f32 v146, v146, v70, v71
	v_max3_f32 v146, v146, v72, v73
	v_max3_f32 v146, v146, v74, v75
	v_max3_f32 v146, v146, v76, v77
	v_mfma_f32_32x32x16_bf16 v[16:31], v[154:157], v[204:207], v[16:31]
	v_max3_f32 v146, v146, v78, v79
	v_mov_b32_e32 v147, v146
	s_nop 1
	v_permlane32_swap_b32_e32 v146, v147
	v_max_f32_e32 v147, v147, v147
	v_max_f32_e32 v146, v146, v146
	v_max_f32_e32 v146, v146, v147
	v_sub_f32_e32 v147, v146, v201
	v_cmp_ge_f32_e32 vcc, s87, v147
	v_max_f32_e32 v147, v201, v201
	v_max_f32_e32 v147, v147, v146
	v_mfma_f32_32x32x16_bf16 v[16:31], v[158:161], v[208:211], v[16:31]
	v_sub_f32_e32 v146, v201, v147
	v_mul_f32_e32 v146, 0x3e0293ee, v146
	v_exp_f32_e32 v146, v146
	s_cmp_eq_u64 vcc, exec
	s_cselect_b64 s[42:43], -1, 0
	s_waitcnt vmcnt(0)
	s_barrier
	s_mov_b32 s54, 1
	v_cndmask_b32_e64 v146, v146, 1.0, s[42:43]
	v_cmp_gt_f32_e32 vcc, 1.0, v146
	s_cbranch_vccz .LBB0_464
	s_and_saveexec_b64 s[6:7], s[40:41]
	ds_write_b32 v184, v146 offset:128
	s_or_b64 exec, exec, s[6:7]
	s_waitcnt lgkmcnt(0)
	v_add_u32_e32 v142, v183, v96
	ds_read_b128 v[130:133], v142 offset:224
	ds_read_b128 v[134:137], v142 offset:192
	ds_read_b128 v[138:141], v142 offset:160
	ds_read_b128 v[142:145], v142 offset:128
	s_waitcnt lgkmcnt(3)
	v_pk_mul_f32 v[12:13], v[12:13], v[130:131]
	s_waitcnt lgkmcnt(2)
	v_pk_mul_f32 v[8:9], v[8:9], v[134:135]
	s_waitcnt lgkmcnt(1)
	v_pk_mul_f32 v[4:5], v[4:5], v[138:139]
	v_pk_mul_f32 v[14:15], v[14:15], v[132:133]
	v_pk_mul_f32 v[10:11], v[10:11], v[136:137]
	v_pk_mul_f32 v[6:7], v[6:7], v[140:141]
	s_waitcnt lgkmcnt(0)
	v_pk_mul_f32 v[2:3], v[2:3], v[144:145]
	v_pk_mul_f32 v[0:1], v[0:1], v[142:143]
	v_pk_mul_f32 v[60:61], v[60:61], v[130:131]
	v_pk_mul_f32 v[56:57], v[56:57], v[134:135]
	v_pk_mul_f32 v[52:53], v[52:53], v[138:139]
	v_pk_mul_f32 v[62:63], v[62:63], v[132:133]
	v_pk_mul_f32 v[58:59], v[58:59], v[136:137]
	v_pk_mul_f32 v[54:55], v[54:55], v[140:141]
	v_pk_mul_f32 v[50:51], v[50:51], v[144:145]
	v_pk_mul_f32 v[48:49], v[48:49], v[142:143]
	v_pk_mul_f32 v[44:45], v[44:45], v[130:131]
	v_pk_mul_f32 v[40:41], v[40:41], v[134:135]
	v_pk_mul_f32 v[36:37], v[36:37], v[138:139]
	v_pk_mul_f32 v[46:47], v[46:47], v[132:133]
	v_pk_mul_f32 v[42:43], v[42:43], v[136:137]
	v_pk_mul_f32 v[38:39], v[38:39], v[140:141]
	v_pk_mul_f32 v[34:35], v[34:35], v[144:145]
	v_pk_mul_f32 v[32:33], v[32:33], v[142:143]
	v_pk_mul_f32 v[28:29], v[28:29], v[130:131]
	v_pk_mul_f32 v[24:25], v[24:25], v[134:135]
	v_pk_mul_f32 v[20:21], v[20:21], v[138:139]
	v_pk_mul_f32 v[30:31], v[30:31], v[132:133]
	v_pk_mul_f32 v[26:27], v[26:27], v[136:137]
	v_pk_mul_f32 v[22:23], v[22:23], v[140:141]
	v_pk_mul_f32 v[18:19], v[18:19], v[144:145]
	v_pk_mul_f32 v[16:17], v[16:17], v[142:143]

; __device__ __forceinline__ void finishSM(f32x16& p0, f32x16& p1, float alpha, float& l_reg, bf16x8& pa0, bf16x8& pa1, bf16x8& pa2, bf16x8& pa3) {
;   for (int r = 0; r < 16; ++r) p1[r] = __builtin_amdgcn_exp2f(p1[r]);
;   float ps = 0; for (int r = 0; r < 16; ++r) ps += p0[r]; for (int r = 0; r < 16; ++r) ps += p1[r];
;   { auto rr = __builtin_amdgcn_permlane32_swap(__float_as_uint(ps), __float_as_uint(ps), false, false);
;     ps = __uint_as_float(rr[0]) + __uint_as_float(rr[1]); }
;   l_reg = l_reg * alpha + ps;
;     ...
;   PK4(p0, 0, pa0); PK4(p0, 8, pa1); PK4(p1, 0, pa2); PK4(p1, 8, pa3);
; template <bool HALF> __device__ __forceinline__ void qkt(f32x16& p0, f32x16& p1, const char* Ks, const bf16x8* qr, int r32, int hi, int koff) {
;   p0 = f32x16{}; p1 = f32x16{};
;   for (int d0 = 0; d0 < (HALF ? 4 : 8); ++d0) { int cb = (d0 * 16 + hi * 8) * 2 + koff;
;     bf16x8 b0 = *reinterpret_cast<const bf16x8*>(Ks + KSWZ(r32, cb));
;     bf16x8 b1 = *reinterpret_cast<const bf16x8*>(Ks + KSWZ(32 + r32, cb));
;     p0 = __builtin_amdgcn_mfma_f32_32x32x16_bf16(b0, qr[d0], p0, 0, 0, 0);
;     p1 = __builtin_amdgcn_mfma_f32_32x32x16_bf16(b1, qr[d0], p1, 0, 0, 0); }
.LBB0_466:
	ds_read_b128 v[64:67], v192 offset:49152
	ds_read_b128 v[68:71], v192 offset:57344
	v_exp_f32_e32 v118, v140
	v_exp_f32_e32 v119, v141
	v_exp_f32_e32 v120, v136
	s_waitcnt lgkmcnt(1)
	v_mfma_f32_32x32x16_bf16 v[80:95], v[64:67], v[98:101], 0
	v_exp_f32_e32 v121, v137
	v_exp_f32_e32 v122, v130
	v_exp_f32_e32 v123, v131
	s_waitcnt lgkmcnt(0)
	v_mfma_f32_32x32x16_bf16 v[64:79], v[68:71], v[98:101], 0
	ds_read_b128 v[98:101], v193 offset:49152
	ds_read_b128 v[114:117], v193 offset:57344
	s_waitcnt lgkmcnt(1)
	v_mfma_f32_32x32x16_bf16 v[80:95], v[98:101], v[106:109], v[80:95]
	s_add_i32 m0, s53, 0x4000
	s_nop 0
	global_load_lds_dwordx4 v234, s[50:51]
	s_add_i32 m0, s53, 0x4400
	s_nop 0
	global_load_lds_dwordx4 v235, s[50:51]
	s_waitcnt lgkmcnt(0)
	v_mfma_f32_32x32x16_bf16 v[64:79], v[114:117], v[106:109], v[64:79]
	ds_read_b128 v[98:101], v195 offset:49152
	ds_read_b128 v[106:109], v195 offset:57344
	v_exp_f32_e32 v114, v134
	v_exp_f32_e32 v115, v135
	v_exp_f32_e32 v116, v132
	v_exp_f32_e32 v117, v133
	s_waitcnt lgkmcnt(1)
	v_mfma_f32_32x32x16_bf16 v[80:95], v[98:101], v[110:113], v[80:95]
	s_waitcnt lgkmcnt(0)
	v_mfma_f32_32x32x16_bf16 v[64:79], v[106:109], v[110:113], v[64:79]
	ds_read_b128 v[98:101], v194 offset:49152
	ds_read_b128 v[106:109], v194 offset:57344
	v_exp_f32_e32 v110, v142
	v_exp_f32_e32 v111, v143
	v_exp_f32_e32 v112, v138
	v_exp_f32_e32 v113, v139
	s_waitcnt lgkmcnt(1)
	v_mfma_f32_32x32x16_bf16 v[80:95], v[98:101], v[102:105], v[80:95]
	v_add_f32_e32 v98, 0, v147
	v_add_f32_e32 v98, v160, v98
	v_add_f32_e32 v98, v148, v98
	v_add_f32_e32 v98, v161, v98
	v_add_f32_e32 v98, v149, v98
	v_add_f32_e32 v98, v170, v98
	v_add_f32_e32 v98, v159, v98
	v_add_f32_e32 v98, v171, v98
	v_add_f32_e32 v98, v151, v98
	v_add_f32_e32 v98, v155, v98
	v_add_f32_e32 v98, v152, v98
	v_add_f32_e32 v98, v156, v98
	s_waitcnt lgkmcnt(0)
	v_mfma_f32_32x32x16_bf16 v[64:79], v[106:109], v[102:105], v[64:79]
	v_exp_f32_e32 v108, v144
	v_add_f32_e32 v98, v153, v98
	v_exp_f32_e32 v109, v145
	v_add_f32_e32 v98, v157, v98
	v_add_f32_e32 v98, v154, v98
	v_add_f32_e32 v98, v158, v98
	v_add_f32_e32 v98, v108, v98
	v_add_f32_e32 v98, v109, v98
	v_add_f32_e32 v98, v110, v98
	v_add_f32_e32 v98, v111, v98
	v_add_f32_e32 v98, v112, v98
	v_add_f32_e32 v98, v113, v98
	v_add_f32_e32 v98, v114, v98
	v_add_f32_e32 v98, v115, v98
	v_add_f32_e32 v98, v116, v98
	v_add_f32_e32 v98, v117, v98
	v_add_f32_e32 v98, v118, v98
	v_add_f32_e32 v98, v119, v98
	v_add_f32_e32 v98, v120, v98
	v_add_f32_e32 v98, v121, v98
	v_add_f32_e32 v98, v122, v98
	v_add_f32_e32 v98, v123, v98
	v_mov_b32_e32 v99, v98
	v_cvt_pk_bf16_f32 v100, v147, v160
	v_cvt_pk_bf16_f32 v101, v148, v161
	v_cvt_pk_bf16_f32 v102, v149, v170
	v_cvt_pk_bf16_f32 v103, v159, v171
	s_nop 1
	v_permlane32_swap_b32_e32 v98, v99
	v_permlane32_swap_b32_e32 v100, v102
	v_permlane32_swap_b32_e32 v101, v103
	v_cvt_pk_bf16_f32 v104, v151, v155
	v_cvt_pk_bf16_f32 v105, v152, v156
	v_cvt_pk_bf16_f32 v106, v153, v157
	v_cvt_pk_bf16_f32 v107, v154, v158
	v_cvt_pk_bf16_f32 v108, v108, v109
	v_cvt_pk_bf16_f32 v109, v110, v111
	v_cvt_pk_bf16_f32 v110, v112, v113
	v_cvt_pk_bf16_f32 v111, v114, v115
	v_cvt_pk_bf16_f32 v112, v116, v117
	v_cvt_pk_bf16_f32 v113, v118, v119
	v_cvt_pk_bf16_f32 v114, v120, v121
	v_cvt_pk_bf16_f32 v115, v122, v123
	s_nop 0
	v_permlane32_swap_b32_e32 v104, v106
	v_permlane32_swap_b32_e32 v105, v107
	v_permlane32_swap_b32_e32 v108, v110
	v_permlane32_swap_b32_e32 v109, v111
	v_permlane32_swap_b32_e32 v112, v114
	v_permlane32_swap_b32_e32 v113, v115
	ds_read_b64_tr_b16 v[116:117], v187 offset:0
	ds_read_b64_tr_b16 v[118:119], v187 offset:0x800
	ds_read_b64_tr_b16 v[120:121], v187 offset:0x1000
	ds_read_b64_tr_b16 v[122:123], v187 offset:0x1800
	ds_read_b64_tr_b16 v[124:125], v187 offset:0x2000
	ds_read_b64_tr_b16 v[126:127], v187 offset:0x2800
	ds_read_b64_tr_b16 v[128:129], v187 offset:0x3000
	ds_read_b64_tr_b16 v[130:131], v187 offset:0x3800
	s_waitcnt lgkmcnt(0)
	s_nop 0
	v_mfma_f32_32x32x16_bf16 v[0:15], v[100:103], v[116:119], v[0:15]
	ds_read_b64_tr_b16 v[116:117], v187 offset:0x200
	ds_read_b64_tr_b16 v[118:119], v187 offset:0xa00
	v_mfma_f32_32x32x16_bf16 v[0:15], v[104:107], v[120:123], v[0:15]
	ds_read_b64_tr_b16 v[120:121], v187 offset:0x1200
	ds_read_b64_tr_b16 v[122:123], v187 offset:0x1a00
	v_mfma_f32_32x32x16_bf16 v[0:15], v[108:111], v[124:127], v[0:15]
	ds_read_b64_tr_b16 v[124:125], v187 offset:0x2200
	ds_read_b64_tr_b16 v[126:127], v187 offset:0x2a00
	v_mfma_f32_32x32x16_bf16 v[0:15], v[112:115], v[128:131], v[0:15]
	ds_read_b64_tr_b16 v[128:129], v187 offset:0x3200
	ds_read_b64_tr_b16 v[130:131], v187 offset:0x3a00
	s_waitcnt lgkmcnt(0)
; #define SBAR() __builtin_amdgcn_sched_barrier(0)
; __device__ __forceinline__ void partialSM(f32x16& p0, f32x16& p1, float& m_reg, float& mn, float& alpha) {
;     ...
;   float pmax = p0[0]; for (int r = 1; r < 16; ++r) pmax = fmaxf(pmax, p0[r]); for (int r = 0; r < 16; ++r) pmax = fmaxf(pmax, p1[r]);
;   { auto rr = __builtin_amdgcn_permlane32_swap(__float_as_uint(pmax), __float_as_uint(pmax), false, false);
;     pmax = fmaxf(__uint_as_float(rr[0]), __uint_as_float(rr[1])); }
;   if (__builtin_expect(__all(pmax - m_reg <= THR / SCALE), 1)) { mn = m_reg; alpha = 1.f; }
;   else { mn = fmaxf(m_reg, pmax); alpha = __builtin_amdgcn_exp2f((m_reg - mn) * C); m_reg = mn; }
; template <int D0> __device__ __forceinline__ void pv_one(f32x16& od, int vb, bf16x8 pa0, bf16x8 pa1, bf16x8 pa2, bf16x8 pa3) {
;   const s16x4 l0 = tr_read<v_rd_off(D0, 0, 0)>(vb), h0 = tr_read<v_rd_off(D0, 0, 1)>(vb), l1 = tr_read<v_rd_off(D0, 1, 0)>(vb), h1 = tr_read<v_rd_off(D0, 1, 1)>(vb);
;   const s16x4 l2 = tr_read<v_rd_off(D0, 2, 0)>(vb), h2 = tr_read<v_rd_off(D0, 2, 1)>(vb), l3 = tr_read<v_rd_off(D0, 3, 0)>(vb), h3 = tr_read<v_rd_off(D0, 3, 1)>(vb);
;   asm volatile("s_waitcnt lgkmcnt(0)" ::: "memory"); SBAR();
;     ...
;   od = __builtin_amdgcn_mfma_f32_32x32x16_bf16(pa0, PK(l0, h0), od, 0, 0, 0);
;   od = __builtin_amdgcn_mfma_f32_32x32x16_bf16(pa1, PK(l1, h1), od, 0, 0, 0);
;   od = __builtin_amdgcn_mfma_f32_32x32x16_bf16(pa2, PK(l2, h2), od, 0, 0, 0);
;   od = __builtin_amdgcn_mfma_f32_32x32x16_bf16(pa3, PK(l3, h3), od, 0, 0, 0);
;     ...
; }
; __device__ __forceinline__ void pv_d0(f32x16* o, int vb, bf16x8 pa0, bf16x8 pa1, bf16x8 pa2, bf16x8 pa3) {
;   pv_one<0>(o[0], vb, pa0, pa1, pa2, pa3); pv_one<1>(o[1], vb, pa0, pa1, pa2, pa3); pv_one<2>(o[2], vb, pa0, pa1, pa2, pa3); pv_one<3>(o[3], vb, pa0, pa1, pa2, pa3);
	v_mfma_f32_32x32x16_bf16 v[48:63], v[100:103], v[116:119], v[48:63]
	ds_read_b64_tr_b16 v[116:117], v187 offset:0x400
	ds_read_b64_tr_b16 v[118:119], v187 offset:0xc00
	v_mfma_f32_32x32x16_bf16 v[48:63], v[104:107], v[120:123], v[48:63]
	ds_read_b64_tr_b16 v[120:121], v187 offset:0x1400
	ds_read_b64_tr_b16 v[122:123], v187 offset:0x1c00
	v_mfma_f32_32x32x16_bf16 v[48:63], v[108:111], v[124:127], v[48:63]
	ds_read_b64_tr_b16 v[124:125], v187 offset:0x2400
	ds_read_b64_tr_b16 v[126:127], v187 offset:0x2c00
	v_mfma_f32_32x32x16_bf16 v[48:63], v[112:115], v[128:131], v[48:63]
	ds_read_b64_tr_b16 v[128:129], v187 offset:0x3400
	ds_read_b64_tr_b16 v[130:131], v187 offset:0x3c00
	s_waitcnt lgkmcnt(0)
	v_mfma_f32_32x32x16_bf16 v[32:47], v[100:103], v[116:119], v[32:47]
	ds_read_b64_tr_b16 v[116:117], v187 offset:0x600
	ds_read_b64_tr_b16 v[118:119], v187 offset:0xe00
	v_mfma_f32_32x32x16_bf16 v[32:47], v[104:107], v[120:123], v[32:47]
	ds_read_b64_tr_b16 v[120:121], v187 offset:0x1600
	ds_read_b64_tr_b16 v[122:123], v187 offset:0x1e00
	v_mfma_f32_32x32x16_bf16 v[32:47], v[108:111], v[124:127], v[32:47]
	ds_read_b64_tr_b16 v[124:125], v187 offset:0x2600
	ds_read_b64_tr_b16 v[126:127], v187 offset:0x2e00
	v_mfma_f32_32x32x16_bf16 v[32:47], v[112:115], v[128:131], v[32:47]
	ds_read_b64_tr_b16 v[128:129], v187 offset:0x3600
	ds_read_b64_tr_b16 v[130:131], v187 offset:0x3e00
	s_waitcnt lgkmcnt(0)
	v_mfma_f32_32x32x16_bf16 v[16:31], v[100:103], v[116:119], v[16:31]
	v_max_f32_e32 v100, v81, v81
	v_max_f32_e32 v101, v80, v80
	v_max_f32_e32 v100, v101, v100
	v_max3_f32 v100, v100, v82, v83
	v_max3_f32 v100, v100, v84, v85
	v_max3_f32 v100, v100, v86, v87
	v_max3_f32 v100, v100, v88, v89
	v_max3_f32 v100, v100, v90, v91
	v_max3_f32 v100, v100, v92, v93
	v_mfma_f32_32x32x16_bf16 v[16:31], v[104:107], v[120:123], v[16:31]
	v_max3_f32 v100, v100, v94, v95
	v_max3_f32 v100, v100, v64, v65
	v_max3_f32 v100, v100, v66, v67
	v_max3_f32 v100, v100, v68, v69
	v_max3_f32 v100, v100, v70, v71
	v_max3_f32 v100, v100, v72, v73
	v_max3_f32 v100, v100, v74, v75
	v_max3_f32 v100, v100, v76, v77
	v_mfma_f32_32x32x16_bf16 v[16:31], v[108:111], v[124:127], v[16:31]
	v_max3_f32 v100, v100, v78, v79
	v_mov_b32_e32 v101, v100
	s_nop 1
	v_permlane32_swap_b32_e32 v100, v101
	v_max_f32_e32 v101, v101, v101
	v_max_f32_e32 v100, v100, v100
	v_max_f32_e32 v100, v100, v101
	v_sub_f32_e32 v101, v100, v150
	v_cmp_ge_f32_e32 vcc, s87, v101
	v_max_f32_e32 v101, v150, v150
	v_max_f32_e32 v101, v101, v100
	v_mfma_f32_32x32x16_bf16 v[16:31], v[112:115], v[128:131], v[16:31]
	v_sub_f32_e32 v100, v150, v101
	v_mul_f32_e32 v100, 0x3e0293ee, v100
	v_exp_f32_e32 v100, v100
	s_cmp_eq_u64 vcc, exec
	s_cselect_b64 s[42:43], -1, 0
	v_cndmask_b32_e64 v100, v100, 1.0, s[42:43]
	v_cmp_gt_f32_e32 vcc, 1.0, v100
	s_waitcnt vmcnt(0)
	s_barrier
	s_cbranch_vccz .LBB0_470
	s_and_saveexec_b64 s[6:7], s[40:41]
	ds_write_b32 v184, v100 offset:128
	s_or_b64 exec, exec, s[6:7]
	s_waitcnt lgkmcnt(0)
	v_add_u32_e32 v114, v183, v96
	ds_read_b128 v[102:105], v114 offset:224
	ds_read_b128 v[106:109], v114 offset:192
	ds_read_b128 v[110:113], v114 offset:160
	ds_read_b128 v[114:117], v114 offset:128
	s_waitcnt lgkmcnt(3)
	v_pk_mul_f32 v[12:13], v[12:13], v[102:103]
	s_waitcnt lgkmcnt(2)
	v_pk_mul_f32 v[8:9], v[8:9], v[106:107]
	s_waitcnt lgkmcnt(1)
	v_pk_mul_f32 v[4:5], v[4:5], v[110:111]
	v_pk_mul_f32 v[14:15], v[14:15], v[104:105]
	v_pk_mul_f32 v[10:11], v[10:11], v[108:109]
	v_pk_mul_f32 v[6:7], v[6:7], v[112:113]
	s_waitcnt lgkmcnt(0)
	v_pk_mul_f32 v[2:3], v[2:3], v[116:117]
	v_pk_mul_f32 v[0:1], v[0:1], v[114:115]
	v_pk_mul_f32 v[60:61], v[60:61], v[102:103]
	v_pk_mul_f32 v[56:57], v[56:57], v[106:107]
	v_pk_mul_f32 v[52:53], v[52:53], v[110:111]
	v_pk_mul_f32 v[62:63], v[62:63], v[104:105]
	v_pk_mul_f32 v[58:59], v[58:59], v[108:109]
	v_pk_mul_f32 v[54:55], v[54:55], v[112:113]
	v_pk_mul_f32 v[50:51], v[50:51], v[116:117]
	v_pk_mul_f32 v[48:49], v[48:49], v[114:115]
	v_pk_mul_f32 v[44:45], v[44:45], v[102:103]
	v_pk_mul_f32 v[40:41], v[40:41], v[106:107]
	v_pk_mul_f32 v[36:37], v[36:37], v[110:111]
	v_pk_mul_f32 v[46:47], v[46:47], v[104:105]
	v_pk_mul_f32 v[42:43], v[42:43], v[108:109]
	v_pk_mul_f32 v[38:39], v[38:39], v[112:113]
	v_pk_mul_f32 v[34:35], v[34:35], v[116:117]
	v_pk_mul_f32 v[32:33], v[32:33], v[114:115]
	v_pk_mul_f32 v[28:29], v[28:29], v[102:103]
	v_pk_mul_f32 v[24:25], v[24:25], v[106:107]
	v_pk_mul_f32 v[20:21], v[20:21], v[110:111]
	v_pk_mul_f32 v[30:31], v[30:31], v[104:105]
	v_pk_mul_f32 v[26:27], v[26:27], v[108:109]
	v_pk_mul_f32 v[22:23], v[22:23], v[112:113]
	v_pk_mul_f32 v[18:19], v[18:19], v[116:117]
	v_pk_mul_f32 v[16:17], v[16:17], v[114:115]
